# GEMM K-loops: lgkmcnt(0) waits in front of MFMAs that do not use the outstanding LDS reads dropped / moved down to the first user (P8, P9)
# baseline (speedup 1.0000x reference)
.LBB0_191:
	s_ashr_i32 s61, s60, 31
	s_lshl_b64 s[62:63], s[60:61], 19
	s_add_u32 s62, s12, s62
	s_addc_u32 s63, s13, s63
	s_ashr_i32 s59, s58, 31
	s_lshl_b64 s[64:65], s[58:59], 19
	s_add_u32 s64, s14, s64
	s_addc_u32 s65, s15, s65
	s_andn2_b64 vcc, exec, s[30:31]
	s_cbranch_vccnz .LBB0_195
	v_cmp_lt_i64_e32 vcc, s[68:69], v[142:143]
	s_and_b64 s[68:69], vcc, exec
	s_cselect_b32 s9, s63, s11
	s_cselect_b32 s59, s62, s10
	s_cselect_b32 s61, s65, s67
	s_cselect_b32 s86, s64, s66
	s_add_u32 s10, s10, 0x40080
	s_addc_u32 s11, s11, 0
	s_add_u32 s87, s66, 0x100
	s_addc_u32 s88, s67, 0
	s_mov_b32 s66, 0
	s_waitcnt vmcnt(0)
	v_add_u32_e32 v154, s77, v157
	ds_read_b128 v[146:149], v154
	ds_read_b128 v[150:153], v154 offset:1024
	ds_read_b128 v[164:167], v154 offset:2048
	ds_read_b128 v[168:171], v154 offset:3072
	s_add_i32 s89, s66, 2
	s_add_u32 s67, s10, 0xfffc0080
	s_addc_u32 s68, s11, -1
	s_cmp_eq_u32 s75, s66
	s_cselect_b32 s66, s86, s87
	s_cselect_b32 s69, s9, s68
	s_cselect_b32 s68, s59, s67
	s_cselect_b32 s67, s61, s88
	v_lshl_add_u64 v[206:207], s[10:11], 0, v[138:139]
	s_add_i32 m0, s52, 0xc000
	ds_read_b128 v[172:175], v159
	ds_read_b128 v[176:179], v159 offset:1024
	ds_read_b128 v[180:183], v159 offset:2048
	ds_read_b128 v[184:187], v159 offset:3072
	ds_read_b128 v[188:191], v159 offset:4096
	ds_read_b128 v[192:195], v159 offset:5120
	ds_read_b128 v[198:201], v159 offset:6144
	ds_read_b128 v[202:205], v159 offset:7168
	global_load_lds_dwordx4 v[206:207], off
	v_lshl_add_u64 v[206:207], s[10:11], 0, v[140:141]
	s_add_i32 m0, s52, 0xe000
	s_nop 0
	global_load_lds_dwordx4 v[206:207], off
	s_waitcnt lgkmcnt(8)
	s_barrier
	s_setprio 1
	s_waitcnt lgkmcnt(0)
	v_mfma_i32_16x16x64_i8 v[62:65], v[146:149], v[172:175], 0
	v_mfma_i32_16x16x64_i8 v[58:61], v[164:167], v[172:175], 0
	v_mfma_i32_16x16x64_i8 v[54:57], v[146:149], v[180:183], 0
	v_mfma_i32_16x16x64_i8 v[50:53], v[164:167], v[180:183], 0
	v_mfma_i32_16x16x64_i8 v[46:49], v[146:149], v[188:191], 0
	v_mfma_i32_16x16x64_i8 v[42:45], v[164:167], v[188:191], 0
	v_mfma_i32_16x16x64_i8 v[38:41], v[146:149], v[198:201], 0
	v_mfma_i32_16x16x64_i8 v[34:37], v[164:167], v[198:201], 0
	v_mfma_i32_16x16x64_i8 v[62:65], v[150:153], v[176:179], v[62:65]
	v_mfma_i32_16x16x64_i8 v[58:61], v[168:171], v[176:179], v[58:61]
	v_mfma_i32_16x16x64_i8 v[54:57], v[150:153], v[184:187], v[54:57]
	v_mfma_i32_16x16x64_i8 v[50:53], v[168:171], v[184:187], v[50:53]
	v_mfma_i32_16x16x64_i8 v[46:49], v[150:153], v[192:195], v[46:49]
	v_mfma_i32_16x16x64_i8 v[42:45], v[168:171], v[192:195], v[42:45]
	v_mfma_i32_16x16x64_i8 v[38:41], v[150:153], v[202:205], v[38:41]
	v_mfma_i32_16x16x64_i8 v[34:37], v[168:171], v[202:205], v[34:37]
	s_setprio 0
	s_barrier
	s_add_i32 s90, s77, s4
	v_add_u32_e32 v154, s78, v157
	v_lshl_add_u64 v[222:223], s[66:67], 0, v[134:135]
	s_mov_b32 m0, s90
	ds_read_b128 v[206:209], v154
	ds_read_b128 v[210:213], v154 offset:1024
	ds_read_b128 v[214:217], v154 offset:2048
	ds_read_b128 v[218:221], v154 offset:3072
	global_load_lds_dwordx4 v[222:223], off
	v_lshl_add_u64 v[224:225], s[66:67], 0, v[130:131]
	s_add_i32 m0, s90, 0x2000
	s_nop 0
	global_load_lds_dwordx4 v[224:225], off
	s_barrier
	s_setprio 1
	s_waitcnt lgkmcnt(0)
	v_mfma_i32_16x16x64_i8 v[126:129], v[206:209], v[172:175], 0
	v_mfma_i32_16x16x64_i8 v[122:125], v[214:217], v[172:175], 0
	ds_read_b128 v[172:175], v159 offset:16384
	v_mfma_i32_16x16x64_i8 v[118:121], v[206:209], v[180:183], 0
	v_mfma_i32_16x16x64_i8 v[114:117], v[214:217], v[180:183], 0
	ds_read_b128 v[180:183], v159 offset:18432
	v_mfma_i32_16x16x64_i8 v[110:113], v[206:209], v[188:191], 0
	v_mfma_i32_16x16x64_i8 v[106:109], v[214:217], v[188:191], 0
	ds_read_b128 v[188:191], v159 offset:20480
	v_mfma_i32_16x16x64_i8 v[102:105], v[206:209], v[198:201], 0
	v_mfma_i32_16x16x64_i8 v[98:101], v[214:217], v[198:201], 0
	ds_read_b128 v[198:201], v159 offset:22528
	v_mfma_i32_16x16x64_i8 v[126:129], v[210:213], v[176:179], v[126:129]
	v_mfma_i32_16x16x64_i8 v[122:125], v[218:221], v[176:179], v[122:125]
	ds_read_b128 v[176:179], v159 offset:17408
	v_mfma_i32_16x16x64_i8 v[118:121], v[210:213], v[184:187], v[118:121]
	v_mfma_i32_16x16x64_i8 v[114:117], v[218:221], v[184:187], v[114:117]
	ds_read_b128 v[184:187], v159 offset:19456
	v_mfma_i32_16x16x64_i8 v[110:113], v[210:213], v[192:195], v[110:113]
	v_mfma_i32_16x16x64_i8 v[106:109], v[218:221], v[192:195], v[106:109]
	ds_read_b128 v[192:195], v159 offset:21504
	v_mfma_i32_16x16x64_i8 v[102:105], v[210:213], v[202:205], v[102:105]
	v_mfma_i32_16x16x64_i8 v[98:101], v[218:221], v[202:205], v[98:101]
	ds_read_b128 v[202:205], v159 offset:23552
	s_setprio 0
	s_mov_b32 m0, s52
	v_lshl_add_u64 v[226:227], s[68:69], 0, v[136:137]
	s_barrier
	global_load_lds_dwordx4 v[226:227], off
	v_lshl_add_u64 v[228:229], s[68:69], 0, v[132:133]
	s_mov_b32 m0, s53
	s_nop 0
	global_load_lds_dwordx4 v[228:229], off
	s_barrier
	s_setprio 1
	s_waitcnt lgkmcnt(0)
	v_mfma_i32_16x16x64_i8 v[30:33], v[146:149], v[172:175], 0
	v_mfma_i32_16x16x64_i8 v[26:29], v[164:167], v[172:175], 0
	v_mfma_i32_16x16x64_i8 v[22:25], v[146:149], v[180:183], 0
	v_mfma_i32_16x16x64_i8 v[18:21], v[164:167], v[180:183], 0
	v_mfma_i32_16x16x64_i8 v[14:17], v[146:149], v[188:191], 0
	v_mfma_i32_16x16x64_i8 v[10:13], v[164:167], v[188:191], 0
	v_mfma_i32_16x16x64_i8 v[6:9], v[146:149], v[198:201], 0
	v_mfma_i32_16x16x64_i8 v[2:5], v[164:167], v[198:201], 0
	v_mfma_i32_16x16x64_i8 v[30:33], v[150:153], v[176:179], v[30:33]
	v_mfma_i32_16x16x64_i8 v[26:29], v[168:171], v[176:179], v[26:29]
	v_mfma_i32_16x16x64_i8 v[22:25], v[150:153], v[184:187], v[22:25]
	v_mfma_i32_16x16x64_i8 v[18:21], v[168:171], v[184:187], v[18:21]
	v_mfma_i32_16x16x64_i8 v[14:17], v[150:153], v[192:195], v[14:17]
	v_mfma_i32_16x16x64_i8 v[10:13], v[168:171], v[192:195], v[10:13]
	v_mfma_i32_16x16x64_i8 v[6:9], v[150:153], v[202:205], v[6:9]
	v_mfma_i32_16x16x64_i8 v[2:5], v[168:171], v[202:205], v[2:5]
	s_setprio 0
	s_barrier
	s_add_u32 s90, s66, 0x40000
	s_addc_u32 s91, s67, 0
	s_add_i32 s92, s78, s4
	v_lshl_add_u64 v[146:147], s[90:91], 0, v[134:135]
	s_mov_b32 m0, s92
	s_nop 0
	global_load_lds_dwordx4 v[146:147], off
	v_lshl_add_u64 v[146:147], s[90:91], 0, v[130:131]
	s_add_i32 m0, s92, 0x2000
	s_nop 0
	global_load_lds_dwordx4 v[146:147], off
	s_waitcnt vmcnt(6)
	s_barrier
	s_setprio 1
	v_mfma_i32_16x16x64_i8 v[94:97], v[206:209], v[172:175], 0
	v_mfma_i32_16x16x64_i8 v[90:93], v[214:217], v[172:175], 0
	ds_read_b128 v[172:175], v159 offset:32768
	v_mfma_i32_16x16x64_i8 v[86:89], v[206:209], v[180:183], 0
	v_mfma_i32_16x16x64_i8 v[82:85], v[214:217], v[180:183], 0
	ds_read_b128 v[180:183], v159 offset:34816
	v_mfma_i32_16x16x64_i8 v[78:81], v[206:209], v[188:191], 0
	v_mfma_i32_16x16x64_i8 v[74:77], v[214:217], v[188:191], 0
	ds_read_b128 v[188:191], v159 offset:36864
	v_mfma_i32_16x16x64_i8 v[70:73], v[206:209], v[198:201], 0
	v_mfma_i32_16x16x64_i8 v[66:69], v[214:217], v[198:201], 0
	ds_read_b128 v[198:201], v159 offset:38912
	v_mfma_i32_16x16x64_i8 v[94:97], v[210:213], v[176:179], v[94:97]
	v_mfma_i32_16x16x64_i8 v[90:93], v[218:221], v[176:179], v[90:93]
	ds_read_b128 v[176:179], v159 offset:33792
	v_mfma_i32_16x16x64_i8 v[86:89], v[210:213], v[184:187], v[86:89]
	v_mfma_i32_16x16x64_i8 v[82:85], v[218:221], v[184:187], v[82:85]
	ds_read_b128 v[184:187], v159 offset:35840
	v_mfma_i32_16x16x64_i8 v[78:81], v[210:213], v[192:195], v[78:81]
	v_mfma_i32_16x16x64_i8 v[74:77], v[218:221], v[192:195], v[74:77]
	ds_read_b128 v[192:195], v159 offset:37888
	v_mfma_i32_16x16x64_i8 v[70:73], v[210:213], v[202:205], v[70:73]
	v_mfma_i32_16x16x64_i8 v[66:69], v[218:221], v[202:205], v[66:69]
	ds_read_b128 v[202:205], v159 offset:39936
	s_setprio 0
	s_add_i32 s90, 0, 0x18000
	v_add_u32_e32 v154, s90, v157
	s_barrier
	ds_read_b128 v[146:149], v154
	ds_read_b128 v[150:153], v154 offset:1024
	ds_read_b128 v[164:167], v154 offset:2048
	ds_read_b128 v[168:171], v154 offset:3072
	s_add_u32 s68, s68, 0x40000
	s_addc_u32 s69, s69, 0
	s_mov_b32 m0, s54
	v_lshl_add_u64 v[206:207], s[68:69], 0, v[136:137]
	global_load_lds_dwordx4 v[206:207], off
	v_lshl_add_u64 v[206:207], s[68:69], 0, v[132:133]
	s_mov_b32 m0, s55
	s_nop 0
	global_load_lds_dwordx4 v[206:207], off
	s_waitcnt lgkmcnt(8)
	s_barrier
	s_setprio 1
	s_waitcnt lgkmcnt(0)
	v_mfma_i32_16x16x64_i8 v[62:65], v[146:149], v[172:175], v[62:65]
	v_mfma_i32_16x16x64_i8 v[58:61], v[164:167], v[172:175], v[58:61]
	v_mfma_i32_16x16x64_i8 v[54:57], v[146:149], v[180:183], v[54:57]
	v_mfma_i32_16x16x64_i8 v[50:53], v[164:167], v[180:183], v[50:53]
	v_mfma_i32_16x16x64_i8 v[46:49], v[146:149], v[188:191], v[46:49]
	v_mfma_i32_16x16x64_i8 v[42:45], v[164:167], v[188:191], v[42:45]
	v_mfma_i32_16x16x64_i8 v[38:41], v[146:149], v[198:201], v[38:41]
	v_mfma_i32_16x16x64_i8 v[34:37], v[164:167], v[198:201], v[34:37]
	v_mfma_i32_16x16x64_i8 v[62:65], v[150:153], v[176:179], v[62:65]
	v_mfma_i32_16x16x64_i8 v[58:61], v[168:171], v[176:179], v[58:61]
	v_mfma_i32_16x16x64_i8 v[54:57], v[150:153], v[184:187], v[54:57]
	v_mfma_i32_16x16x64_i8 v[50:53], v[168:171], v[184:187], v[50:53]
	v_mfma_i32_16x16x64_i8 v[46:49], v[150:153], v[192:195], v[46:49]
	v_mfma_i32_16x16x64_i8 v[42:45], v[168:171], v[192:195], v[42:45]
	v_mfma_i32_16x16x64_i8 v[38:41], v[150:153], v[202:205], v[38:41]
	v_mfma_i32_16x16x64_i8 v[34:37], v[168:171], v[202:205], v[34:37]
	s_setprio 0
	s_barrier
	s_add_i32 s68, 0, 0x1c000
	s_add_i32 s69, s90, s4
	v_add_u32_e32 v154, s68, v157
	v_lshl_add_u64 v[222:223], v[222:223], 0, s[28:29]
	s_mov_b32 m0, s69
	ds_read_b128 v[206:209], v154
	ds_read_b128 v[210:213], v154 offset:1024
	ds_read_b128 v[214:217], v154 offset:2048
	ds_read_b128 v[218:221], v154 offset:3072
	global_load_lds_dwordx4 v[222:223], off
	v_lshl_add_u64 v[222:223], v[224:225], 0, s[28:29]
	s_add_i32 m0, s69, 0x2000
	s_nop 0
	global_load_lds_dwordx4 v[222:223], off
	s_barrier
	s_setprio 1
	s_waitcnt lgkmcnt(0)
	v_mfma_i32_16x16x64_i8 v[126:129], v[206:209], v[172:175], v[126:129]
	v_mfma_i32_16x16x64_i8 v[122:125], v[214:217], v[172:175], v[122:125]
	ds_read_b128 v[172:175], v159 offset:49152
	v_mfma_i32_16x16x64_i8 v[118:121], v[206:209], v[180:183], v[118:121]
	v_mfma_i32_16x16x64_i8 v[114:117], v[214:217], v[180:183], v[114:117]
	ds_read_b128 v[180:183], v159 offset:51200
	v_mfma_i32_16x16x64_i8 v[110:113], v[206:209], v[188:191], v[110:113]
	v_mfma_i32_16x16x64_i8 v[106:109], v[214:217], v[188:191], v[106:109]
	ds_read_b128 v[188:191], v159 offset:53248
	v_mfma_i32_16x16x64_i8 v[102:105], v[206:209], v[198:201], v[102:105]
	v_mfma_i32_16x16x64_i8 v[98:101], v[214:217], v[198:201], v[98:101]
	ds_read_b128 v[198:201], v159 offset:55296
	v_mfma_i32_16x16x64_i8 v[126:129], v[210:213], v[176:179], v[126:129]
	v_mfma_i32_16x16x64_i8 v[122:125], v[218:221], v[176:179], v[122:125]
	ds_read_b128 v[176:179], v159 offset:50176
	v_mfma_i32_16x16x64_i8 v[118:121], v[210:213], v[184:187], v[118:121]
	v_mfma_i32_16x16x64_i8 v[114:117], v[218:221], v[184:187], v[114:117]
	ds_read_b128 v[184:187], v159 offset:52224
	v_mfma_i32_16x16x64_i8 v[110:113], v[210:213], v[192:195], v[110:113]
	v_mfma_i32_16x16x64_i8 v[106:109], v[218:221], v[192:195], v[106:109]
	ds_read_b128 v[192:195], v159 offset:54272
	v_mfma_i32_16x16x64_i8 v[102:105], v[210:213], v[202:205], v[102:105]
	v_mfma_i32_16x16x64_i8 v[98:101], v[218:221], v[202:205], v[98:101]
	ds_read_b128 v[202:205], v159 offset:56320
	s_setprio 0
	s_mov_b32 m0, s73
	v_lshl_add_u64 v[222:223], v[226:227], 0, s[28:29]
	s_barrier
	global_load_lds_dwordx4 v[222:223], off
	v_lshl_add_u64 v[222:223], v[228:229], 0, s[28:29]
	s_mov_b32 m0, s74
	s_nop 0
	global_load_lds_dwordx4 v[222:223], off
	s_barrier
	s_setprio 1
	s_waitcnt lgkmcnt(0)
	v_mfma_i32_16x16x64_i8 v[30:33], v[146:149], v[172:175], v[30:33]
	v_mfma_i32_16x16x64_i8 v[26:29], v[164:167], v[172:175], v[26:29]
	v_mfma_i32_16x16x64_i8 v[22:25], v[146:149], v[180:183], v[22:25]
	v_mfma_i32_16x16x64_i8 v[18:21], v[164:167], v[180:183], v[18:21]
	v_mfma_i32_16x16x64_i8 v[14:17], v[146:149], v[188:191], v[14:17]
	v_mfma_i32_16x16x64_i8 v[10:13], v[164:167], v[188:191], v[10:13]
	v_mfma_i32_16x16x64_i8 v[6:9], v[146:149], v[198:201], v[6:9]
	v_mfma_i32_16x16x64_i8 v[2:5], v[164:167], v[198:201], v[2:5]
	v_mfma_i32_16x16x64_i8 v[30:33], v[150:153], v[176:179], v[30:33]
	v_mfma_i32_16x16x64_i8 v[26:29], v[168:171], v[176:179], v[26:29]
	v_mfma_i32_16x16x64_i8 v[22:25], v[150:153], v[184:187], v[22:25]
	v_mfma_i32_16x16x64_i8 v[18:21], v[168:171], v[184:187], v[18:21]
	v_mfma_i32_16x16x64_i8 v[14:17], v[150:153], v[192:195], v[14:17]
	v_mfma_i32_16x16x64_i8 v[10:13], v[168:171], v[192:195], v[10:13]
	v_mfma_i32_16x16x64_i8 v[6:9], v[150:153], v[202:205], v[6:9]
	v_mfma_i32_16x16x64_i8 v[2:5], v[168:171], v[202:205], v[2:5]
	s_setprio 0
	s_barrier
	s_add_u32 s66, s66, 0x40080
	s_addc_u32 s67, s67, 0
	s_add_i32 s68, s68, s4
	v_lshl_add_u64 v[146:147], s[66:67], 0, v[134:135]
	s_mov_b32 m0, s68
	s_nop 0
	global_load_lds_dwordx4 v[146:147], off
	v_lshl_add_u64 v[146:147], s[66:67], 0, v[130:131]
	s_add_i32 m0, s68, 0x2000
	s_nop 0
	global_load_lds_dwordx4 v[146:147], off
	s_waitcnt vmcnt(6)
	s_barrier
	s_setprio 1
	v_mfma_i32_16x16x64_i8 v[94:97], v[206:209], v[172:175], v[94:97]
	v_mfma_i32_16x16x64_i8 v[90:93], v[214:217], v[172:175], v[90:93]
	v_mfma_i32_16x16x64_i8 v[86:89], v[206:209], v[180:183], v[86:89]
	v_mfma_i32_16x16x64_i8 v[82:85], v[214:217], v[180:183], v[82:85]
	v_mfma_i32_16x16x64_i8 v[78:81], v[206:209], v[188:191], v[78:81]
	v_mfma_i32_16x16x64_i8 v[74:77], v[214:217], v[188:191], v[74:77]
	v_mfma_i32_16x16x64_i8 v[70:73], v[206:209], v[198:201], v[70:73]
	v_mfma_i32_16x16x64_i8 v[66:69], v[214:217], v[198:201], v[66:69]
	v_mfma_i32_16x16x64_i8 v[94:97], v[210:213], v[176:179], v[94:97]
	v_mfma_i32_16x16x64_i8 v[90:93], v[218:221], v[176:179], v[90:93]
	v_mfma_i32_16x16x64_i8 v[86:89], v[210:213], v[184:187], v[86:89]
	v_mfma_i32_16x16x64_i8 v[82:85], v[218:221], v[184:187], v[82:85]
	v_mfma_i32_16x16x64_i8 v[78:81], v[210:213], v[192:195], v[78:81]
	v_mfma_i32_16x16x64_i8 v[74:77], v[218:221], v[192:195], v[74:77]
	v_mfma_i32_16x16x64_i8 v[70:73], v[210:213], v[202:205], v[70:73]
	v_mfma_i32_16x16x64_i8 v[66:69], v[218:221], v[202:205], v[66:69]
	s_setprio 0
	s_add_u32 s10, s10, 0x100
	s_addc_u32 s11, s11, 0
	s_add_u32 s87, s87, 0x100
	s_addc_u32 s88, s88, 0
	s_cmp_ge_i32 s89, s1
	s_mov_b32 s66, s89
	s_barrier
	s_cbranch_scc0 .LBB0_193
	s_branch .Lmy_pl0_exit
.LBB0_193:
	s_waitcnt vmcnt(0)
	v_add_u32_e32 v154, s77, v157
	ds_read_b128 v[146:149], v154
	ds_read_b128 v[150:153], v154 offset:1024
	ds_read_b128 v[164:167], v154 offset:2048
	ds_read_b128 v[168:171], v154 offset:3072
	s_add_i32 s89, s66, 2
	s_add_u32 s67, s10, 0xfffc0080
	s_addc_u32 s68, s11, -1
	s_cmp_eq_u32 s75, s66
	s_cselect_b32 s66, s86, s87
	s_cselect_b32 s69, s9, s68
	s_cselect_b32 s68, s59, s67
	s_cselect_b32 s67, s61, s88
	v_lshl_add_u64 v[206:207], s[10:11], 0, v[138:139]
	s_add_i32 m0, s52, 0xc000
	ds_read_b128 v[172:175], v159
	ds_read_b128 v[176:179], v159 offset:1024
	ds_read_b128 v[180:183], v159 offset:2048
	ds_read_b128 v[184:187], v159 offset:3072
	ds_read_b128 v[188:191], v159 offset:4096
	ds_read_b128 v[192:195], v159 offset:5120
	ds_read_b128 v[198:201], v159 offset:6144
	ds_read_b128 v[202:205], v159 offset:7168
	global_load_lds_dwordx4 v[206:207], off
	v_lshl_add_u64 v[206:207], s[10:11], 0, v[140:141]
	s_add_i32 m0, s52, 0xe000
	s_nop 0
	global_load_lds_dwordx4 v[206:207], off
	s_waitcnt lgkmcnt(8)
	s_barrier
	s_setprio 1
	s_waitcnt lgkmcnt(0)
	v_mfma_i32_16x16x64_i8 v[62:65], v[146:149], v[172:175], v[62:65]
	v_mfma_i32_16x16x64_i8 v[58:61], v[164:167], v[172:175], v[58:61]
	v_mfma_i32_16x16x64_i8 v[54:57], v[146:149], v[180:183], v[54:57]
	v_mfma_i32_16x16x64_i8 v[50:53], v[164:167], v[180:183], v[50:53]
	v_mfma_i32_16x16x64_i8 v[46:49], v[146:149], v[188:191], v[46:49]
	v_mfma_i32_16x16x64_i8 v[42:45], v[164:167], v[188:191], v[42:45]
	v_mfma_i32_16x16x64_i8 v[38:41], v[146:149], v[198:201], v[38:41]
	v_mfma_i32_16x16x64_i8 v[34:37], v[164:167], v[198:201], v[34:37]
	v_mfma_i32_16x16x64_i8 v[62:65], v[150:153], v[176:179], v[62:65]
	v_mfma_i32_16x16x64_i8 v[58:61], v[168:171], v[176:179], v[58:61]
	v_mfma_i32_16x16x64_i8 v[54:57], v[150:153], v[184:187], v[54:57]
	v_mfma_i32_16x16x64_i8 v[50:53], v[168:171], v[184:187], v[50:53]
	v_mfma_i32_16x16x64_i8 v[46:49], v[150:153], v[192:195], v[46:49]
	v_mfma_i32_16x16x64_i8 v[42:45], v[168:171], v[192:195], v[42:45]
	v_mfma_i32_16x16x64_i8 v[38:41], v[150:153], v[202:205], v[38:41]
	v_mfma_i32_16x16x64_i8 v[34:37], v[168:171], v[202:205], v[34:37]
	s_setprio 0
	s_barrier
	s_add_i32 s90, s77, s4
	v_add_u32_e32 v154, s78, v157
	v_lshl_add_u64 v[222:223], s[66:67], 0, v[134:135]
	s_mov_b32 m0, s90
	ds_read_b128 v[206:209], v154
	ds_read_b128 v[210:213], v154 offset:1024
	ds_read_b128 v[214:217], v154 offset:2048
	ds_read_b128 v[218:221], v154 offset:3072
	global_load_lds_dwordx4 v[222:223], off
	v_lshl_add_u64 v[224:225], s[66:67], 0, v[130:131]
	s_add_i32 m0, s90, 0x2000
	s_nop 0
	global_load_lds_dwordx4 v[224:225], off
	s_barrier
	s_setprio 1
	s_waitcnt lgkmcnt(0)
	v_mfma_i32_16x16x64_i8 v[126:129], v[206:209], v[172:175], v[126:129]
	v_mfma_i32_16x16x64_i8 v[122:125], v[214:217], v[172:175], v[122:125]
	ds_read_b128 v[172:175], v159 offset:16384
	v_mfma_i32_16x16x64_i8 v[118:121], v[206:209], v[180:183], v[118:121]
	v_mfma_i32_16x16x64_i8 v[114:117], v[214:217], v[180:183], v[114:117]
	ds_read_b128 v[180:183], v159 offset:18432
	v_mfma_i32_16x16x64_i8 v[110:113], v[206:209], v[188:191], v[110:113]
	v_mfma_i32_16x16x64_i8 v[106:109], v[214:217], v[188:191], v[106:109]
	ds_read_b128 v[188:191], v159 offset:20480
	v_mfma_i32_16x16x64_i8 v[102:105], v[206:209], v[198:201], v[102:105]
	v_mfma_i32_16x16x64_i8 v[98:101], v[214:217], v[198:201], v[98:101]
	ds_read_b128 v[198:201], v159 offset:22528
	v_mfma_i32_16x16x64_i8 v[126:129], v[210:213], v[176:179], v[126:129]
	v_mfma_i32_16x16x64_i8 v[122:125], v[218:221], v[176:179], v[122:125]
	ds_read_b128 v[176:179], v159 offset:17408
	v_mfma_i32_16x16x64_i8 v[118:121], v[210:213], v[184:187], v[118:121]
	v_mfma_i32_16x16x64_i8 v[114:117], v[218:221], v[184:187], v[114:117]
	ds_read_b128 v[184:187], v159 offset:19456
	v_mfma_i32_16x16x64_i8 v[110:113], v[210:213], v[192:195], v[110:113]
	v_mfma_i32_16x16x64_i8 v[106:109], v[218:221], v[192:195], v[106:109]
	ds_read_b128 v[192:195], v159 offset:21504
	v_mfma_i32_16x16x64_i8 v[102:105], v[210:213], v[202:205], v[102:105]
	v_mfma_i32_16x16x64_i8 v[98:101], v[218:221], v[202:205], v[98:101]
	ds_read_b128 v[202:205], v159 offset:23552
	s_setprio 0
	s_mov_b32 m0, s52
	v_lshl_add_u64 v[226:227], s[68:69], 0, v[136:137]
	s_barrier
	global_load_lds_dwordx4 v[226:227], off
	v_lshl_add_u64 v[228:229], s[68:69], 0, v[132:133]
	s_mov_b32 m0, s53
	s_nop 0
	global_load_lds_dwordx4 v[228:229], off
	s_barrier
	s_setprio 1
	s_waitcnt lgkmcnt(0)
	v_mfma_i32_16x16x64_i8 v[30:33], v[146:149], v[172:175], v[30:33]
	v_mfma_i32_16x16x64_i8 v[26:29], v[164:167], v[172:175], v[26:29]
	v_mfma_i32_16x16x64_i8 v[22:25], v[146:149], v[180:183], v[22:25]
	v_mfma_i32_16x16x64_i8 v[18:21], v[164:167], v[180:183], v[18:21]
	v_mfma_i32_16x16x64_i8 v[14:17], v[146:149], v[188:191], v[14:17]
	v_mfma_i32_16x16x64_i8 v[10:13], v[164:167], v[188:191], v[10:13]
	v_mfma_i32_16x16x64_i8 v[6:9], v[146:149], v[198:201], v[6:9]
	v_mfma_i32_16x16x64_i8 v[2:5], v[164:167], v[198:201], v[2:5]
	v_mfma_i32_16x16x64_i8 v[30:33], v[150:153], v[176:179], v[30:33]
	v_mfma_i32_16x16x64_i8 v[26:29], v[168:171], v[176:179], v[26:29]
	v_mfma_i32_16x16x64_i8 v[22:25], v[150:153], v[184:187], v[22:25]
	v_mfma_i32_16x16x64_i8 v[18:21], v[168:171], v[184:187], v[18:21]
	v_mfma_i32_16x16x64_i8 v[14:17], v[150:153], v[192:195], v[14:17]
	v_mfma_i32_16x16x64_i8 v[10:13], v[168:171], v[192:195], v[10:13]
	v_mfma_i32_16x16x64_i8 v[6:9], v[150:153], v[202:205], v[6:9]
	v_mfma_i32_16x16x64_i8 v[2:5], v[168:171], v[202:205], v[2:5]
	s_setprio 0
	s_barrier
	s_add_u32 s90, s66, 0x40000
	s_addc_u32 s91, s67, 0
	s_add_i32 s92, s78, s4
	v_lshl_add_u64 v[146:147], s[90:91], 0, v[134:135]
	s_mov_b32 m0, s92
	s_nop 0
	global_load_lds_dwordx4 v[146:147], off
	v_lshl_add_u64 v[146:147], s[90:91], 0, v[130:131]
	s_add_i32 m0, s92, 0x2000
	s_nop 0
	global_load_lds_dwordx4 v[146:147], off
	s_waitcnt vmcnt(6)
	s_barrier
	s_setprio 1
	v_mfma_i32_16x16x64_i8 v[94:97], v[206:209], v[172:175], v[94:97]
	v_mfma_i32_16x16x64_i8 v[90:93], v[214:217], v[172:175], v[90:93]
	ds_read_b128 v[172:175], v159 offset:32768
	v_mfma_i32_16x16x64_i8 v[86:89], v[206:209], v[180:183], v[86:89]
	v_mfma_i32_16x16x64_i8 v[82:85], v[214:217], v[180:183], v[82:85]
	ds_read_b128 v[180:183], v159 offset:34816
	v_mfma_i32_16x16x64_i8 v[78:81], v[206:209], v[188:191], v[78:81]
	v_mfma_i32_16x16x64_i8 v[74:77], v[214:217], v[188:191], v[74:77]
	ds_read_b128 v[188:191], v159 offset:36864
	v_mfma_i32_16x16x64_i8 v[70:73], v[206:209], v[198:201], v[70:73]
	v_mfma_i32_16x16x64_i8 v[66:69], v[214:217], v[198:201], v[66:69]
	ds_read_b128 v[198:201], v159 offset:38912
	v_mfma_i32_16x16x64_i8 v[94:97], v[210:213], v[176:179], v[94:97]
	v_mfma_i32_16x16x64_i8 v[90:93], v[218:221], v[176:179], v[90:93]
	ds_read_b128 v[176:179], v159 offset:33792
	v_mfma_i32_16x16x64_i8 v[86:89], v[210:213], v[184:187], v[86:89]
	v_mfma_i32_16x16x64_i8 v[82:85], v[218:221], v[184:187], v[82:85]
	ds_read_b128 v[184:187], v159 offset:35840
	v_mfma_i32_16x16x64_i8 v[78:81], v[210:213], v[192:195], v[78:81]
	v_mfma_i32_16x16x64_i8 v[74:77], v[218:221], v[192:195], v[74:77]
	ds_read_b128 v[192:195], v159 offset:37888
	v_mfma_i32_16x16x64_i8 v[70:73], v[210:213], v[202:205], v[70:73]
	v_mfma_i32_16x16x64_i8 v[66:69], v[218:221], v[202:205], v[66:69]
	ds_read_b128 v[202:205], v159 offset:39936
	s_setprio 0
	s_add_i32 s90, 0, 0x18000
	v_add_u32_e32 v154, s90, v157
	s_barrier
	ds_read_b128 v[146:149], v154
	ds_read_b128 v[150:153], v154 offset:1024
	ds_read_b128 v[164:167], v154 offset:2048
	ds_read_b128 v[168:171], v154 offset:3072
	s_add_u32 s68, s68, 0x40000
	s_addc_u32 s69, s69, 0
	s_mov_b32 m0, s54
	v_lshl_add_u64 v[206:207], s[68:69], 0, v[136:137]
	global_load_lds_dwordx4 v[206:207], off
	v_lshl_add_u64 v[206:207], s[68:69], 0, v[132:133]
	s_mov_b32 m0, s55
	s_nop 0
	global_load_lds_dwordx4 v[206:207], off
	s_waitcnt lgkmcnt(8)
	s_barrier
	s_setprio 1
	s_waitcnt lgkmcnt(0)
	v_mfma_i32_16x16x64_i8 v[62:65], v[146:149], v[172:175], v[62:65]
	v_mfma_i32_16x16x64_i8 v[58:61], v[164:167], v[172:175], v[58:61]
	v_mfma_i32_16x16x64_i8 v[54:57], v[146:149], v[180:183], v[54:57]
	v_mfma_i32_16x16x64_i8 v[50:53], v[164:167], v[180:183], v[50:53]
	v_mfma_i32_16x16x64_i8 v[46:49], v[146:149], v[188:191], v[46:49]
	v_mfma_i32_16x16x64_i8 v[42:45], v[164:167], v[188:191], v[42:45]
	v_mfma_i32_16x16x64_i8 v[38:41], v[146:149], v[198:201], v[38:41]
	v_mfma_i32_16x16x64_i8 v[34:37], v[164:167], v[198:201], v[34:37]
	v_mfma_i32_16x16x64_i8 v[62:65], v[150:153], v[176:179], v[62:65]
	v_mfma_i32_16x16x64_i8 v[58:61], v[168:171], v[176:179], v[58:61]
	v_mfma_i32_16x16x64_i8 v[54:57], v[150:153], v[184:187], v[54:57]
	v_mfma_i32_16x16x64_i8 v[50:53], v[168:171], v[184:187], v[50:53]
	v_mfma_i32_16x16x64_i8 v[46:49], v[150:153], v[192:195], v[46:49]
	v_mfma_i32_16x16x64_i8 v[42:45], v[168:171], v[192:195], v[42:45]
	v_mfma_i32_16x16x64_i8 v[38:41], v[150:153], v[202:205], v[38:41]
	v_mfma_i32_16x16x64_i8 v[34:37], v[168:171], v[202:205], v[34:37]
	s_setprio 0
	s_barrier
	s_add_i32 s68, 0, 0x1c000
	s_add_i32 s69, s90, s4
	v_add_u32_e32 v154, s68, v157
	v_lshl_add_u64 v[222:223], v[222:223], 0, s[28:29]
	s_mov_b32 m0, s69
	ds_read_b128 v[206:209], v154
	ds_read_b128 v[210:213], v154 offset:1024
	ds_read_b128 v[214:217], v154 offset:2048
	ds_read_b128 v[218:221], v154 offset:3072
	global_load_lds_dwordx4 v[222:223], off
	v_lshl_add_u64 v[222:223], v[224:225], 0, s[28:29]
	s_add_i32 m0, s69, 0x2000
	s_nop 0
	global_load_lds_dwordx4 v[222:223], off
	s_barrier
	s_setprio 1
	s_waitcnt lgkmcnt(0)
	v_mfma_i32_16x16x64_i8 v[126:129], v[206:209], v[172:175], v[126:129]
	v_mfma_i32_16x16x64_i8 v[122:125], v[214:217], v[172:175], v[122:125]
	ds_read_b128 v[172:175], v159 offset:49152
	v_mfma_i32_16x16x64_i8 v[118:121], v[206:209], v[180:183], v[118:121]
	v_mfma_i32_16x16x64_i8 v[114:117], v[214:217], v[180:183], v[114:117]
	ds_read_b128 v[180:183], v159 offset:51200
	v_mfma_i32_16x16x64_i8 v[110:113], v[206:209], v[188:191], v[110:113]
	v_mfma_i32_16x16x64_i8 v[106:109], v[214:217], v[188:191], v[106:109]
	ds_read_b128 v[188:191], v159 offset:53248
	v_mfma_i32_16x16x64_i8 v[102:105], v[206:209], v[198:201], v[102:105]
	v_mfma_i32_16x16x64_i8 v[98:101], v[214:217], v[198:201], v[98:101]
	ds_read_b128 v[198:201], v159 offset:55296
	v_mfma_i32_16x16x64_i8 v[126:129], v[210:213], v[176:179], v[126:129]
	v_mfma_i32_16x16x64_i8 v[122:125], v[218:221], v[176:179], v[122:125]
	ds_read_b128 v[176:179], v159 offset:50176
	v_mfma_i32_16x16x64_i8 v[118:121], v[210:213], v[184:187], v[118:121]
	v_mfma_i32_16x16x64_i8 v[114:117], v[218:221], v[184:187], v[114:117]
	ds_read_b128 v[184:187], v159 offset:52224
	v_mfma_i32_16x16x64_i8 v[110:113], v[210:213], v[192:195], v[110:113]
	v_mfma_i32_16x16x64_i8 v[106:109], v[218:221], v[192:195], v[106:109]
	ds_read_b128 v[192:195], v159 offset:54272
	v_mfma_i32_16x16x64_i8 v[102:105], v[210:213], v[202:205], v[102:105]
	v_mfma_i32_16x16x64_i8 v[98:101], v[218:221], v[202:205], v[98:101]
	ds_read_b128 v[202:205], v159 offset:56320
	s_setprio 0
	s_mov_b32 m0, s73
	v_lshl_add_u64 v[222:223], v[226:227], 0, s[28:29]
	s_barrier
	global_load_lds_dwordx4 v[222:223], off
	v_lshl_add_u64 v[222:223], v[228:229], 0, s[28:29]
	s_mov_b32 m0, s74
	s_nop 0
	global_load_lds_dwordx4 v[222:223], off
	s_barrier
	s_setprio 1
	s_waitcnt lgkmcnt(0)
	v_mfma_i32_16x16x64_i8 v[30:33], v[146:149], v[172:175], v[30:33]
	v_mfma_i32_16x16x64_i8 v[26:29], v[164:167], v[172:175], v[26:29]
	v_mfma_i32_16x16x64_i8 v[22:25], v[146:149], v[180:183], v[22:25]
	v_mfma_i32_16x16x64_i8 v[18:21], v[164:167], v[180:183], v[18:21]
	v_mfma_i32_16x16x64_i8 v[14:17], v[146:149], v[188:191], v[14:17]
	v_mfma_i32_16x16x64_i8 v[10:13], v[164:167], v[188:191], v[10:13]
	v_mfma_i32_16x16x64_i8 v[6:9], v[146:149], v[198:201], v[6:9]
	v_mfma_i32_16x16x64_i8 v[2:5], v[164:167], v[198:201], v[2:5]
	v_mfma_i32_16x16x64_i8 v[30:33], v[150:153], v[176:179], v[30:33]
	v_mfma_i32_16x16x64_i8 v[26:29], v[168:171], v[176:179], v[26:29]
	v_mfma_i32_16x16x64_i8 v[22:25], v[150:153], v[184:187], v[22:25]
	v_mfma_i32_16x16x64_i8 v[18:21], v[168:171], v[184:187], v[18:21]
	v_mfma_i32_16x16x64_i8 v[14:17], v[150:153], v[192:195], v[14:17]
	v_mfma_i32_16x16x64_i8 v[10:13], v[168:171], v[192:195], v[10:13]
	v_mfma_i32_16x16x64_i8 v[6:9], v[150:153], v[202:205], v[6:9]
	v_mfma_i32_16x16x64_i8 v[2:5], v[168:171], v[202:205], v[2:5]
	s_setprio 0
	s_barrier
	s_add_u32 s66, s66, 0x40080
	s_addc_u32 s67, s67, 0
	s_add_i32 s68, s68, s4
	v_lshl_add_u64 v[146:147], s[66:67], 0, v[134:135]
	s_mov_b32 m0, s68
	s_nop 0
	global_load_lds_dwordx4 v[146:147], off
	v_lshl_add_u64 v[146:147], s[66:67], 0, v[130:131]
	s_add_i32 m0, s68, 0x2000
	s_nop 0
	global_load_lds_dwordx4 v[146:147], off
	s_waitcnt vmcnt(6)
	s_barrier
	s_setprio 1
	v_mfma_i32_16x16x64_i8 v[94:97], v[206:209], v[172:175], v[94:97]
	v_mfma_i32_16x16x64_i8 v[90:93], v[214:217], v[172:175], v[90:93]
	v_mfma_i32_16x16x64_i8 v[86:89], v[206:209], v[180:183], v[86:89]
	v_mfma_i32_16x16x64_i8 v[82:85], v[214:217], v[180:183], v[82:85]
	v_mfma_i32_16x16x64_i8 v[78:81], v[206:209], v[188:191], v[78:81]
	v_mfma_i32_16x16x64_i8 v[74:77], v[214:217], v[188:191], v[74:77]
	v_mfma_i32_16x16x64_i8 v[70:73], v[206:209], v[198:201], v[70:73]
	v_mfma_i32_16x16x64_i8 v[66:69], v[214:217], v[198:201], v[66:69]
	v_mfma_i32_16x16x64_i8 v[94:97], v[210:213], v[176:179], v[94:97]
	v_mfma_i32_16x16x64_i8 v[90:93], v[218:221], v[176:179], v[90:93]
	v_mfma_i32_16x16x64_i8 v[86:89], v[210:213], v[184:187], v[86:89]
	v_mfma_i32_16x16x64_i8 v[82:85], v[218:221], v[184:187], v[82:85]
	v_mfma_i32_16x16x64_i8 v[78:81], v[210:213], v[192:195], v[78:81]
	v_mfma_i32_16x16x64_i8 v[74:77], v[218:221], v[192:195], v[74:77]
	v_mfma_i32_16x16x64_i8 v[70:73], v[210:213], v[202:205], v[70:73]
	v_mfma_i32_16x16x64_i8 v[66:69], v[218:221], v[202:205], v[66:69]
	s_setprio 0
	s_add_u32 s10, s10, 0x100
	s_addc_u32 s11, s11, 0
	s_add_u32 s87, s87, 0x100
	s_addc_u32 s88, s88, 0
	s_cmp_ge_i32 s89, s1
	s_mov_b32 s66, s89
	s_barrier
	s_cbranch_scc0 .LBB0_193

.LBB0_962:
	s_ashr_i32 s27, s26, 31
	s_lshl_b64 s[28:29], s[26:27], 20
	s_add_u32 s28, s10, s28
	s_addc_u32 s29, s11, s29
	s_ashr_i32 s25, s24, 31
	s_lshl_b64 s[30:31], s[24:25], 20
	s_add_u32 s30, s14, s30
	v_cmp_lt_i64_e64 s[8:9], s[8:9], v[158:159]
	s_addc_u32 s31, s15, s31
	s_andn2_b64 vcc, exec, s[20:21]
	s_cbranch_vccnz .LBB0_954
	s_and_b64 s[8:9], s[8:9], exec
	s_cselect_b32 s25, s29, s39
	s_cselect_b32 s27, s28, s38
	s_cselect_b32 s51, s31, s37
	s_cselect_b32 s52, s30, s36
	s_add_u32 s8, s38, 0x80080
	s_addc_u32 s9, s39, 0
	s_add_u32 s53, s36, 0x100
	v_mov_b32_e32 v2, 0
	s_addc_u32 s54, s37, 0
	s_mov_b32 s36, 0
	ds_read_b128 v[130:133], v172
	ds_read_b128 v[134:137], v172 offset:1024
	ds_read_b128 v[138:141], v172 offset:2048
	ds_read_b128 v[142:145], v172 offset:3072
	s_add_i32 s55, s36, 2
	s_add_u32 s37, s8, 0xfff80080
	s_addc_u32 s38, s9, -1
	s_cmp_eq_u32 s46, s36
	s_cselect_b32 s36, s52, s53
	s_cselect_b32 s39, s25, s38
	s_cselect_b32 s38, s27, s37
	s_cselect_b32 s37, s51, s54
	v_lshl_add_u64 v[200:201], s[8:9], 0, v[154:155]
	s_add_i32 m0, s23, 0xc000
	ds_read_b128 v[162:165], v173
	ds_read_b128 v[166:169], v173 offset:1024
	ds_read_b128 v[176:179], v173 offset:2048
	ds_read_b128 v[180:183], v173 offset:3072
	ds_read_b128 v[184:187], v173 offset:4096
	ds_read_b128 v[188:191], v173 offset:5120
	ds_read_b128 v[192:195], v173 offset:6144
	ds_read_b128 v[196:199], v173 offset:7168
	global_load_lds_dwordx4 v[200:201], off
	v_lshl_add_u64 v[200:201], s[8:9], 0, v[156:157]
	s_add_i32 m0, s23, 0xe000
	s_nop 0
	global_load_lds_dwordx4 v[200:201], off
	s_waitcnt lgkmcnt(8)
	s_barrier
	s_setprio 1
	s_waitcnt lgkmcnt(0)
	v_mfma_f32_16x16x32_bf16 v[126:129], v[130:133], v[162:165], 0
	ds_read_b128 v[200:203], v174
	ds_read_b128 v[204:207], v174 offset:1024
	ds_read_b128 v[208:211], v174 offset:2048
	ds_read_b128 v[214:217], v174 offset:3072
	v_mfma_f32_16x16x32_bf16 v[122:125], v[138:141], v[162:165], 0
	v_mfma_f32_16x16x32_bf16 v[110:113], v[130:133], v[176:179], 0
	v_mfma_f32_16x16x32_bf16 v[106:109], v[138:141], v[176:179], 0
	v_mfma_f32_16x16x32_bf16 v[94:97], v[130:133], v[184:187], 0
	v_mfma_f32_16x16x32_bf16 v[90:93], v[138:141], v[184:187], 0
	v_mfma_f32_16x16x32_bf16 v[78:81], v[130:133], v[192:195], 0
	v_mfma_f32_16x16x32_bf16 v[74:77], v[138:141], v[192:195], 0
	v_mfma_f32_16x16x32_bf16 v[126:129], v[134:137], v[166:169], v[126:129]
	v_mfma_f32_16x16x32_bf16 v[122:125], v[142:145], v[166:169], v[122:125]
	v_mfma_f32_16x16x32_bf16 v[110:113], v[134:137], v[180:183], v[110:113]
	v_mfma_f32_16x16x32_bf16 v[106:109], v[142:145], v[180:183], v[106:109]
	v_mfma_f32_16x16x32_bf16 v[94:97], v[134:137], v[188:191], v[94:97]
	v_mfma_f32_16x16x32_bf16 v[90:93], v[142:145], v[188:191], v[90:93]
	v_mfma_f32_16x16x32_bf16 v[78:81], v[134:137], v[196:199], v[78:81]
	v_mfma_f32_16x16x32_bf16 v[74:77], v[142:145], v[196:199], v[74:77]
	s_setprio 0
	s_barrier
	s_add_i32 s56, s48, s5
	v_lshl_add_u64 v[218:219], s[36:37], 0, v[148:149]
	s_mov_b32 m0, s56
	global_load_lds_dwordx4 v[218:219], off
	v_lshl_add_u64 v[220:221], s[36:37], 0, v[152:153]
	s_add_i32 m0, s56, 0x2000
	s_nop 0
	global_load_lds_dwordx4 v[220:221], off
	s_barrier
	s_setprio 1
	s_waitcnt lgkmcnt(0)
	v_mfma_f32_16x16x32_bf16 v[118:121], v[200:203], v[162:165], 0
	v_mfma_f32_16x16x32_bf16 v[114:117], v[208:211], v[162:165], 0
	ds_read_b128 v[162:165], v173 offset:16384
	v_mfma_f32_16x16x32_bf16 v[102:105], v[200:203], v[176:179], 0
	v_mfma_f32_16x16x32_bf16 v[98:101], v[208:211], v[176:179], 0
	ds_read_b128 v[176:179], v173 offset:18432
	v_mfma_f32_16x16x32_bf16 v[86:89], v[200:203], v[184:187], 0
	v_mfma_f32_16x16x32_bf16 v[82:85], v[208:211], v[184:187], 0
	ds_read_b128 v[184:187], v173 offset:20480
	v_mfma_f32_16x16x32_bf16 v[70:73], v[200:203], v[192:195], 0
	v_mfma_f32_16x16x32_bf16 v[66:69], v[208:211], v[192:195], 0
	ds_read_b128 v[192:195], v173 offset:22528
	v_mfma_f32_16x16x32_bf16 v[118:121], v[204:207], v[166:169], v[118:121]
	v_mfma_f32_16x16x32_bf16 v[114:117], v[214:217], v[166:169], v[114:117]
	ds_read_b128 v[166:169], v173 offset:17408
	v_mfma_f32_16x16x32_bf16 v[102:105], v[204:207], v[180:183], v[102:105]
	v_mfma_f32_16x16x32_bf16 v[98:101], v[214:217], v[180:183], v[98:101]
	ds_read_b128 v[180:183], v173 offset:19456
	v_mfma_f32_16x16x32_bf16 v[86:89], v[204:207], v[188:191], v[86:89]
	v_mfma_f32_16x16x32_bf16 v[82:85], v[214:217], v[188:191], v[82:85]
	ds_read_b128 v[188:191], v173 offset:21504
	v_mfma_f32_16x16x32_bf16 v[70:73], v[204:207], v[196:199], v[70:73]
	v_mfma_f32_16x16x32_bf16 v[66:69], v[214:217], v[196:199], v[66:69]
	ds_read_b128 v[196:199], v173 offset:23552
	s_setprio 0
	s_mov_b32 m0, s23
	v_lshl_add_u64 v[222:223], s[38:39], 0, v[146:147]
	s_barrier
	global_load_lds_dwordx4 v[222:223], off
	v_lshl_add_u64 v[224:225], s[38:39], 0, v[150:151]
	s_mov_b32 m0, s33
	s_nop 0
	global_load_lds_dwordx4 v[224:225], off
	s_barrier
	s_setprio 1
	s_waitcnt lgkmcnt(0)
	v_mfma_f32_16x16x32_bf16 v[62:65], v[130:133], v[162:165], 0
	v_mfma_f32_16x16x32_bf16 v[58:61], v[138:141], v[162:165], 0
	v_mfma_f32_16x16x32_bf16 v[46:49], v[130:133], v[176:179], 0
	v_mfma_f32_16x16x32_bf16 v[42:45], v[138:141], v[176:179], 0
	v_mfma_f32_16x16x32_bf16 v[30:33], v[130:133], v[184:187], 0
	v_mfma_f32_16x16x32_bf16 v[26:29], v[138:141], v[184:187], 0
	v_mfma_f32_16x16x32_bf16 v[14:17], v[130:133], v[192:195], 0
	v_mfma_f32_16x16x32_bf16 v[10:13], v[138:141], v[192:195], 0
	v_mfma_f32_16x16x32_bf16 v[62:65], v[134:137], v[166:169], v[62:65]
	v_mfma_f32_16x16x32_bf16 v[58:61], v[142:145], v[166:169], v[58:61]
	v_mfma_f32_16x16x32_bf16 v[46:49], v[134:137], v[180:183], v[46:49]
	v_mfma_f32_16x16x32_bf16 v[42:45], v[142:145], v[180:183], v[42:45]
	v_mfma_f32_16x16x32_bf16 v[30:33], v[134:137], v[188:191], v[30:33]
	v_mfma_f32_16x16x32_bf16 v[26:29], v[142:145], v[188:191], v[26:29]
	v_mfma_f32_16x16x32_bf16 v[14:17], v[134:137], v[196:199], v[14:17]
	v_mfma_f32_16x16x32_bf16 v[10:13], v[142:145], v[196:199], v[10:13]
	s_setprio 0
	s_barrier
	s_add_u32 s56, s36, 0x80000
	s_addc_u32 s57, s37, 0
	s_add_i32 s58, s49, s5
	v_lshl_add_u64 v[130:131], s[56:57], 0, v[148:149]
	s_mov_b32 m0, s58
	s_nop 0
	global_load_lds_dwordx4 v[130:131], off
	v_lshl_add_u64 v[130:131], s[56:57], 0, v[152:153]
	s_add_i32 m0, s58, 0x2000
	s_nop 0
	global_load_lds_dwordx4 v[130:131], off
	s_waitcnt vmcnt(6)
	s_barrier
	s_setprio 1
	v_mfma_f32_16x16x32_bf16 v[54:57], v[200:203], v[162:165], 0
	v_mfma_f32_16x16x32_bf16 v[50:53], v[208:211], v[162:165], 0
	ds_read_b128 v[162:165], v173 offset:32768
	v_mfma_f32_16x16x32_bf16 v[38:41], v[200:203], v[176:179], 0
	v_mfma_f32_16x16x32_bf16 v[34:37], v[208:211], v[176:179], 0
	ds_read_b128 v[176:179], v173 offset:34816
	v_mfma_f32_16x16x32_bf16 v[22:25], v[200:203], v[184:187], 0
	v_mfma_f32_16x16x32_bf16 v[18:21], v[208:211], v[184:187], 0
	ds_read_b128 v[184:187], v173 offset:36864
	v_mfma_f32_16x16x32_bf16 v[6:9], v[200:203], v[192:195], 0
	v_mfma_f32_16x16x32_bf16 v[2:5], v[208:211], v[192:195], 0
	ds_read_b128 v[192:195], v173 offset:38912
	v_mfma_f32_16x16x32_bf16 v[54:57], v[204:207], v[166:169], v[54:57]
	v_mfma_f32_16x16x32_bf16 v[50:53], v[214:217], v[166:169], v[50:53]
	ds_read_b128 v[166:169], v173 offset:33792
	v_mfma_f32_16x16x32_bf16 v[38:41], v[204:207], v[180:183], v[38:41]
	v_mfma_f32_16x16x32_bf16 v[34:37], v[214:217], v[180:183], v[34:37]
	ds_read_b128 v[180:183], v173 offset:35840
	v_mfma_f32_16x16x32_bf16 v[22:25], v[204:207], v[188:191], v[22:25]
	v_mfma_f32_16x16x32_bf16 v[18:21], v[214:217], v[188:191], v[18:21]
	ds_read_b128 v[188:191], v173 offset:37888
	v_mfma_f32_16x16x32_bf16 v[6:9], v[204:207], v[196:199], v[6:9]
	v_mfma_f32_16x16x32_bf16 v[2:5], v[214:217], v[196:199], v[2:5]
	ds_read_b128 v[196:199], v173 offset:39936
	s_setprio 0
	s_add_i32 s56, 0, 0x18000
	v_add_u32_e32 v142, s56, v171
	s_barrier
	ds_read_b128 v[130:133], v142
	ds_read_b128 v[134:137], v142 offset:1024
	ds_read_b128 v[138:141], v142 offset:2048
	ds_read_b128 v[142:145], v142 offset:3072
	s_add_u32 s38, s38, 0x80000
	s_addc_u32 s39, s39, 0
	s_mov_b32 m0, s35
	v_lshl_add_u64 v[200:201], s[38:39], 0, v[146:147]
	global_load_lds_dwordx4 v[200:201], off
	v_lshl_add_u64 v[200:201], s[38:39], 0, v[150:151]
	s_mov_b32 m0, s40
	s_nop 0
	global_load_lds_dwordx4 v[200:201], off
	s_waitcnt lgkmcnt(8)
	s_barrier
	s_setprio 1
	s_waitcnt lgkmcnt(0)
	v_mfma_f32_16x16x32_bf16 v[126:129], v[130:133], v[162:165], v[126:129]
	v_mfma_f32_16x16x32_bf16 v[122:125], v[138:141], v[162:165], v[122:125]
	v_mfma_f32_16x16x32_bf16 v[110:113], v[130:133], v[176:179], v[110:113]
	v_mfma_f32_16x16x32_bf16 v[106:109], v[138:141], v[176:179], v[106:109]
	v_mfma_f32_16x16x32_bf16 v[94:97], v[130:133], v[184:187], v[94:97]
	v_mfma_f32_16x16x32_bf16 v[90:93], v[138:141], v[184:187], v[90:93]
	v_mfma_f32_16x16x32_bf16 v[78:81], v[130:133], v[192:195], v[78:81]
	v_mfma_f32_16x16x32_bf16 v[74:77], v[138:141], v[192:195], v[74:77]
	v_mfma_f32_16x16x32_bf16 v[126:129], v[134:137], v[166:169], v[126:129]
	v_mfma_f32_16x16x32_bf16 v[122:125], v[142:145], v[166:169], v[122:125]
	v_mfma_f32_16x16x32_bf16 v[110:113], v[134:137], v[180:183], v[110:113]
	v_mfma_f32_16x16x32_bf16 v[106:109], v[142:145], v[180:183], v[106:109]
	v_mfma_f32_16x16x32_bf16 v[94:97], v[134:137], v[188:191], v[94:97]
	v_mfma_f32_16x16x32_bf16 v[90:93], v[142:145], v[188:191], v[90:93]
	v_mfma_f32_16x16x32_bf16 v[78:81], v[134:137], v[196:199], v[78:81]
	v_mfma_f32_16x16x32_bf16 v[74:77], v[142:145], v[196:199], v[74:77]
	s_setprio 0
	s_barrier
	s_add_i32 s38, 0, 0x1c000
	s_add_i32 s39, s56, s5
	v_add_u32_e32 v175, s38, v171
	v_lshl_add_u64 v[218:219], v[218:219], 0, s[18:19]
	s_mov_b32 m0, s39
	ds_read_b128 v[200:203], v175
	ds_read_b128 v[204:207], v175 offset:1024
	ds_read_b128 v[208:211], v175 offset:2048
	ds_read_b128 v[214:217], v175 offset:3072
	global_load_lds_dwordx4 v[218:219], off
	v_lshl_add_u64 v[218:219], v[220:221], 0, s[18:19]
	s_add_i32 m0, s39, 0x2000
	s_nop 0
	global_load_lds_dwordx4 v[218:219], off
	s_barrier
	s_setprio 1
	s_waitcnt lgkmcnt(0)
	v_mfma_f32_16x16x32_bf16 v[118:121], v[200:203], v[162:165], v[118:121]
	v_mfma_f32_16x16x32_bf16 v[114:117], v[208:211], v[162:165], v[114:117]
	ds_read_b128 v[162:165], v173 offset:49152
	v_mfma_f32_16x16x32_bf16 v[102:105], v[200:203], v[176:179], v[102:105]
	v_mfma_f32_16x16x32_bf16 v[98:101], v[208:211], v[176:179], v[98:101]
	ds_read_b128 v[176:179], v173 offset:51200
	v_mfma_f32_16x16x32_bf16 v[86:89], v[200:203], v[184:187], v[86:89]
	v_mfma_f32_16x16x32_bf16 v[82:85], v[208:211], v[184:187], v[82:85]
	ds_read_b128 v[184:187], v173 offset:53248
	v_mfma_f32_16x16x32_bf16 v[70:73], v[200:203], v[192:195], v[70:73]
	v_mfma_f32_16x16x32_bf16 v[66:69], v[208:211], v[192:195], v[66:69]
	ds_read_b128 v[192:195], v173 offset:55296
	v_mfma_f32_16x16x32_bf16 v[118:121], v[204:207], v[166:169], v[118:121]
	v_mfma_f32_16x16x32_bf16 v[114:117], v[214:217], v[166:169], v[114:117]
	ds_read_b128 v[166:169], v173 offset:50176
	v_mfma_f32_16x16x32_bf16 v[102:105], v[204:207], v[180:183], v[102:105]
	v_mfma_f32_16x16x32_bf16 v[98:101], v[214:217], v[180:183], v[98:101]
	ds_read_b128 v[180:183], v173 offset:52224
	v_mfma_f32_16x16x32_bf16 v[86:89], v[204:207], v[188:191], v[86:89]
	v_mfma_f32_16x16x32_bf16 v[82:85], v[214:217], v[188:191], v[82:85]
	ds_read_b128 v[188:191], v173 offset:54272
	v_mfma_f32_16x16x32_bf16 v[70:73], v[204:207], v[196:199], v[70:73]
	v_mfma_f32_16x16x32_bf16 v[66:69], v[214:217], v[196:199], v[66:69]
	ds_read_b128 v[196:199], v173 offset:56320
	s_setprio 0
	s_mov_b32 m0, s44
	v_lshl_add_u64 v[218:219], v[222:223], 0, s[18:19]
	s_barrier
	global_load_lds_dwordx4 v[218:219], off
	v_lshl_add_u64 v[218:219], v[224:225], 0, s[18:19]
	s_mov_b32 m0, s45
	s_nop 0
	global_load_lds_dwordx4 v[218:219], off
	s_barrier
	s_setprio 1
	s_waitcnt lgkmcnt(0)
	v_mfma_f32_16x16x32_bf16 v[62:65], v[130:133], v[162:165], v[62:65]
	v_mfma_f32_16x16x32_bf16 v[58:61], v[138:141], v[162:165], v[58:61]
	v_mfma_f32_16x16x32_bf16 v[46:49], v[130:133], v[176:179], v[46:49]
	v_mfma_f32_16x16x32_bf16 v[42:45], v[138:141], v[176:179], v[42:45]
	v_mfma_f32_16x16x32_bf16 v[30:33], v[130:133], v[184:187], v[30:33]
	v_mfma_f32_16x16x32_bf16 v[26:29], v[138:141], v[184:187], v[26:29]
	v_mfma_f32_16x16x32_bf16 v[14:17], v[130:133], v[192:195], v[14:17]
	v_mfma_f32_16x16x32_bf16 v[10:13], v[138:141], v[192:195], v[10:13]
	v_mfma_f32_16x16x32_bf16 v[62:65], v[134:137], v[166:169], v[62:65]
	v_mfma_f32_16x16x32_bf16 v[58:61], v[142:145], v[166:169], v[58:61]
	v_mfma_f32_16x16x32_bf16 v[46:49], v[134:137], v[180:183], v[46:49]
	v_mfma_f32_16x16x32_bf16 v[42:45], v[142:145], v[180:183], v[42:45]
	v_mfma_f32_16x16x32_bf16 v[30:33], v[134:137], v[188:191], v[30:33]
	v_mfma_f32_16x16x32_bf16 v[26:29], v[142:145], v[188:191], v[26:29]
	v_mfma_f32_16x16x32_bf16 v[14:17], v[134:137], v[196:199], v[14:17]
	v_mfma_f32_16x16x32_bf16 v[10:13], v[142:145], v[196:199], v[10:13]
	s_setprio 0
	s_barrier
	s_add_u32 s36, s36, 0x80080
	s_addc_u32 s37, s37, 0
	s_add_i32 s38, s38, s5
	v_lshl_add_u64 v[130:131], s[36:37], 0, v[148:149]
	s_mov_b32 m0, s38
	s_nop 0
	global_load_lds_dwordx4 v[130:131], off
	v_lshl_add_u64 v[130:131], s[36:37], 0, v[152:153]
	s_add_i32 m0, s38, 0x2000
	s_nop 0
	global_load_lds_dwordx4 v[130:131], off
	s_waitcnt vmcnt(6)
	s_barrier
	s_setprio 1
	v_mfma_f32_16x16x32_bf16 v[54:57], v[200:203], v[162:165], v[54:57]
	v_mfma_f32_16x16x32_bf16 v[50:53], v[208:211], v[162:165], v[50:53]
	v_mfma_f32_16x16x32_bf16 v[38:41], v[200:203], v[176:179], v[38:41]
	v_mfma_f32_16x16x32_bf16 v[34:37], v[208:211], v[176:179], v[34:37]
	v_mfma_f32_16x16x32_bf16 v[22:25], v[200:203], v[184:187], v[22:25]
	v_mfma_f32_16x16x32_bf16 v[18:21], v[208:211], v[184:187], v[18:21]
	v_mfma_f32_16x16x32_bf16 v[6:9], v[200:203], v[192:195], v[6:9]
	v_mfma_f32_16x16x32_bf16 v[2:5], v[208:211], v[192:195], v[2:5]
	v_mfma_f32_16x16x32_bf16 v[54:57], v[204:207], v[166:169], v[54:57]
	v_mfma_f32_16x16x32_bf16 v[50:53], v[214:217], v[166:169], v[50:53]
	v_mfma_f32_16x16x32_bf16 v[38:41], v[204:207], v[180:183], v[38:41]
	v_mfma_f32_16x16x32_bf16 v[34:37], v[214:217], v[180:183], v[34:37]
	v_mfma_f32_16x16x32_bf16 v[22:25], v[204:207], v[188:191], v[22:25]
	v_mfma_f32_16x16x32_bf16 v[18:21], v[214:217], v[188:191], v[18:21]
	v_mfma_f32_16x16x32_bf16 v[6:9], v[204:207], v[196:199], v[6:9]
	v_mfma_f32_16x16x32_bf16 v[2:5], v[214:217], v[196:199], v[2:5]
	s_setprio 0
	s_add_u32 s8, s8, 0x100
	s_addc_u32 s9, s9, 0
	s_add_u32 s53, s53, 0x100
	s_addc_u32 s54, s54, 0
	s_cmp_ge_i32 s55, s1
	s_mov_b32 s36, s55
	s_barrier
	s_cbranch_scc0 .LBB0_964
	s_branch .Lmy_pl1_exit
.LBB0_964:
	ds_read_b128 v[130:133], v172
	ds_read_b128 v[134:137], v172 offset:1024
	ds_read_b128 v[138:141], v172 offset:2048
	ds_read_b128 v[142:145], v172 offset:3072
	s_add_i32 s55, s36, 2
	s_add_u32 s37, s8, 0xfff80080
	s_addc_u32 s38, s9, -1
	s_cmp_eq_u32 s46, s36
	s_cselect_b32 s36, s52, s53
	s_cselect_b32 s39, s25, s38
	s_cselect_b32 s38, s27, s37
	s_cselect_b32 s37, s51, s54
	v_lshl_add_u64 v[200:201], s[8:9], 0, v[154:155]
	s_add_i32 m0, s23, 0xc000
	ds_read_b128 v[162:165], v173
	ds_read_b128 v[166:169], v173 offset:1024
	ds_read_b128 v[176:179], v173 offset:2048
	ds_read_b128 v[180:183], v173 offset:3072
	ds_read_b128 v[184:187], v173 offset:4096
	ds_read_b128 v[188:191], v173 offset:5120
	ds_read_b128 v[192:195], v173 offset:6144
	ds_read_b128 v[196:199], v173 offset:7168
	global_load_lds_dwordx4 v[200:201], off
	v_lshl_add_u64 v[200:201], s[8:9], 0, v[156:157]
	s_add_i32 m0, s23, 0xe000
	s_nop 0
	global_load_lds_dwordx4 v[200:201], off
	s_waitcnt lgkmcnt(8)
	s_barrier
	s_setprio 1
	s_waitcnt lgkmcnt(0)
	v_mfma_f32_16x16x32_bf16 v[126:129], v[130:133], v[162:165], v[126:129]
	ds_read_b128 v[200:203], v174
	ds_read_b128 v[204:207], v174 offset:1024
	ds_read_b128 v[208:211], v174 offset:2048
	ds_read_b128 v[214:217], v174 offset:3072
	v_mfma_f32_16x16x32_bf16 v[122:125], v[138:141], v[162:165], v[122:125]
	v_mfma_f32_16x16x32_bf16 v[110:113], v[130:133], v[176:179], v[110:113]
	v_mfma_f32_16x16x32_bf16 v[106:109], v[138:141], v[176:179], v[106:109]
	v_mfma_f32_16x16x32_bf16 v[94:97], v[130:133], v[184:187], v[94:97]
	v_mfma_f32_16x16x32_bf16 v[90:93], v[138:141], v[184:187], v[90:93]
	v_mfma_f32_16x16x32_bf16 v[78:81], v[130:133], v[192:195], v[78:81]
	v_mfma_f32_16x16x32_bf16 v[74:77], v[138:141], v[192:195], v[74:77]
	v_mfma_f32_16x16x32_bf16 v[126:129], v[134:137], v[166:169], v[126:129]
	v_mfma_f32_16x16x32_bf16 v[122:125], v[142:145], v[166:169], v[122:125]
	v_mfma_f32_16x16x32_bf16 v[110:113], v[134:137], v[180:183], v[110:113]
	v_mfma_f32_16x16x32_bf16 v[106:109], v[142:145], v[180:183], v[106:109]
	v_mfma_f32_16x16x32_bf16 v[94:97], v[134:137], v[188:191], v[94:97]
	v_mfma_f32_16x16x32_bf16 v[90:93], v[142:145], v[188:191], v[90:93]
	v_mfma_f32_16x16x32_bf16 v[78:81], v[134:137], v[196:199], v[78:81]
	v_mfma_f32_16x16x32_bf16 v[74:77], v[142:145], v[196:199], v[74:77]
	s_setprio 0
	s_barrier
	s_add_i32 s56, s48, s5
	v_lshl_add_u64 v[218:219], s[36:37], 0, v[148:149]
	s_mov_b32 m0, s56
	global_load_lds_dwordx4 v[218:219], off
	v_lshl_add_u64 v[220:221], s[36:37], 0, v[152:153]
	s_add_i32 m0, s56, 0x2000
	s_nop 0
	global_load_lds_dwordx4 v[220:221], off
	s_barrier
	s_setprio 1
	s_waitcnt lgkmcnt(0)
	v_mfma_f32_16x16x32_bf16 v[118:121], v[200:203], v[162:165], v[118:121]
	v_mfma_f32_16x16x32_bf16 v[114:117], v[208:211], v[162:165], v[114:117]
	ds_read_b128 v[162:165], v173 offset:16384
	v_mfma_f32_16x16x32_bf16 v[102:105], v[200:203], v[176:179], v[102:105]
	v_mfma_f32_16x16x32_bf16 v[98:101], v[208:211], v[176:179], v[98:101]
	ds_read_b128 v[176:179], v173 offset:18432
	v_mfma_f32_16x16x32_bf16 v[86:89], v[200:203], v[184:187], v[86:89]
	v_mfma_f32_16x16x32_bf16 v[82:85], v[208:211], v[184:187], v[82:85]
	ds_read_b128 v[184:187], v173 offset:20480
	v_mfma_f32_16x16x32_bf16 v[70:73], v[200:203], v[192:195], v[70:73]
	v_mfma_f32_16x16x32_bf16 v[66:69], v[208:211], v[192:195], v[66:69]
	ds_read_b128 v[192:195], v173 offset:22528
	v_mfma_f32_16x16x32_bf16 v[118:121], v[204:207], v[166:169], v[118:121]
	v_mfma_f32_16x16x32_bf16 v[114:117], v[214:217], v[166:169], v[114:117]
	ds_read_b128 v[166:169], v173 offset:17408
	v_mfma_f32_16x16x32_bf16 v[102:105], v[204:207], v[180:183], v[102:105]
	v_mfma_f32_16x16x32_bf16 v[98:101], v[214:217], v[180:183], v[98:101]
	ds_read_b128 v[180:183], v173 offset:19456
	v_mfma_f32_16x16x32_bf16 v[86:89], v[204:207], v[188:191], v[86:89]
	v_mfma_f32_16x16x32_bf16 v[82:85], v[214:217], v[188:191], v[82:85]
	ds_read_b128 v[188:191], v173 offset:21504
	v_mfma_f32_16x16x32_bf16 v[70:73], v[204:207], v[196:199], v[70:73]
	v_mfma_f32_16x16x32_bf16 v[66:69], v[214:217], v[196:199], v[66:69]
	ds_read_b128 v[196:199], v173 offset:23552
	s_setprio 0
	s_mov_b32 m0, s23
	v_lshl_add_u64 v[222:223], s[38:39], 0, v[146:147]
	s_barrier
	global_load_lds_dwordx4 v[222:223], off
	v_lshl_add_u64 v[224:225], s[38:39], 0, v[150:151]
	s_mov_b32 m0, s33
	s_nop 0
	global_load_lds_dwordx4 v[224:225], off
	s_barrier
	s_setprio 1
	s_waitcnt lgkmcnt(0)
	v_mfma_f32_16x16x32_bf16 v[62:65], v[130:133], v[162:165], v[62:65]
	v_mfma_f32_16x16x32_bf16 v[58:61], v[138:141], v[162:165], v[58:61]
	v_mfma_f32_16x16x32_bf16 v[46:49], v[130:133], v[176:179], v[46:49]
	v_mfma_f32_16x16x32_bf16 v[42:45], v[138:141], v[176:179], v[42:45]
	v_mfma_f32_16x16x32_bf16 v[30:33], v[130:133], v[184:187], v[30:33]
	v_mfma_f32_16x16x32_bf16 v[26:29], v[138:141], v[184:187], v[26:29]
	v_mfma_f32_16x16x32_bf16 v[14:17], v[130:133], v[192:195], v[14:17]
	v_mfma_f32_16x16x32_bf16 v[10:13], v[138:141], v[192:195], v[10:13]
	v_mfma_f32_16x16x32_bf16 v[62:65], v[134:137], v[166:169], v[62:65]
	v_mfma_f32_16x16x32_bf16 v[58:61], v[142:145], v[166:169], v[58:61]
	v_mfma_f32_16x16x32_bf16 v[46:49], v[134:137], v[180:183], v[46:49]
	v_mfma_f32_16x16x32_bf16 v[42:45], v[142:145], v[180:183], v[42:45]
	v_mfma_f32_16x16x32_bf16 v[30:33], v[134:137], v[188:191], v[30:33]
	v_mfma_f32_16x16x32_bf16 v[26:29], v[142:145], v[188:191], v[26:29]
	v_mfma_f32_16x16x32_bf16 v[14:17], v[134:137], v[196:199], v[14:17]
	v_mfma_f32_16x16x32_bf16 v[10:13], v[142:145], v[196:199], v[10:13]
	s_setprio 0
	s_barrier
	s_add_u32 s56, s36, 0x80000
	s_addc_u32 s57, s37, 0
	s_add_i32 s58, s49, s5
	v_lshl_add_u64 v[130:131], s[56:57], 0, v[148:149]
	s_mov_b32 m0, s58
	s_nop 0
	global_load_lds_dwordx4 v[130:131], off
	v_lshl_add_u64 v[130:131], s[56:57], 0, v[152:153]
	s_add_i32 m0, s58, 0x2000
	s_nop 0
	global_load_lds_dwordx4 v[130:131], off
	s_waitcnt vmcnt(6)
	s_barrier
	s_setprio 1
	v_mfma_f32_16x16x32_bf16 v[54:57], v[200:203], v[162:165], v[54:57]
	v_mfma_f32_16x16x32_bf16 v[50:53], v[208:211], v[162:165], v[50:53]
	ds_read_b128 v[162:165], v173 offset:32768
	v_mfma_f32_16x16x32_bf16 v[38:41], v[200:203], v[176:179], v[38:41]
	v_mfma_f32_16x16x32_bf16 v[34:37], v[208:211], v[176:179], v[34:37]
	ds_read_b128 v[176:179], v173 offset:34816
	v_mfma_f32_16x16x32_bf16 v[22:25], v[200:203], v[184:187], v[22:25]
	v_mfma_f32_16x16x32_bf16 v[18:21], v[208:211], v[184:187], v[18:21]
	ds_read_b128 v[184:187], v173 offset:36864
	v_mfma_f32_16x16x32_bf16 v[6:9], v[200:203], v[192:195], v[6:9]
	v_mfma_f32_16x16x32_bf16 v[2:5], v[208:211], v[192:195], v[2:5]
	ds_read_b128 v[192:195], v173 offset:38912
	v_mfma_f32_16x16x32_bf16 v[54:57], v[204:207], v[166:169], v[54:57]
	v_mfma_f32_16x16x32_bf16 v[50:53], v[214:217], v[166:169], v[50:53]
	ds_read_b128 v[166:169], v173 offset:33792
	v_mfma_f32_16x16x32_bf16 v[38:41], v[204:207], v[180:183], v[38:41]
	v_mfma_f32_16x16x32_bf16 v[34:37], v[214:217], v[180:183], v[34:37]
	ds_read_b128 v[180:183], v173 offset:35840
	v_mfma_f32_16x16x32_bf16 v[22:25], v[204:207], v[188:191], v[22:25]
	v_mfma_f32_16x16x32_bf16 v[18:21], v[214:217], v[188:191], v[18:21]
	ds_read_b128 v[188:191], v173 offset:37888
	v_mfma_f32_16x16x32_bf16 v[6:9], v[204:207], v[196:199], v[6:9]
	v_mfma_f32_16x16x32_bf16 v[2:5], v[214:217], v[196:199], v[2:5]
	ds_read_b128 v[196:199], v173 offset:39936
	s_setprio 0
	s_add_i32 s56, 0, 0x18000
	v_add_u32_e32 v142, s56, v171
	s_barrier
	ds_read_b128 v[130:133], v142
	ds_read_b128 v[134:137], v142 offset:1024
	ds_read_b128 v[138:141], v142 offset:2048
	ds_read_b128 v[142:145], v142 offset:3072
	s_add_u32 s38, s38, 0x80000
	s_addc_u32 s39, s39, 0
	s_mov_b32 m0, s35
	v_lshl_add_u64 v[200:201], s[38:39], 0, v[146:147]
	global_load_lds_dwordx4 v[200:201], off
	v_lshl_add_u64 v[200:201], s[38:39], 0, v[150:151]
	s_mov_b32 m0, s40
	s_nop 0
	global_load_lds_dwordx4 v[200:201], off
	s_waitcnt lgkmcnt(8)
	s_barrier
	s_setprio 1
	s_waitcnt lgkmcnt(0)
	v_mfma_f32_16x16x32_bf16 v[126:129], v[130:133], v[162:165], v[126:129]
	v_mfma_f32_16x16x32_bf16 v[122:125], v[138:141], v[162:165], v[122:125]
	v_mfma_f32_16x16x32_bf16 v[110:113], v[130:133], v[176:179], v[110:113]
	v_mfma_f32_16x16x32_bf16 v[106:109], v[138:141], v[176:179], v[106:109]
	v_mfma_f32_16x16x32_bf16 v[94:97], v[130:133], v[184:187], v[94:97]
	v_mfma_f32_16x16x32_bf16 v[90:93], v[138:141], v[184:187], v[90:93]
	v_mfma_f32_16x16x32_bf16 v[78:81], v[130:133], v[192:195], v[78:81]
	v_mfma_f32_16x16x32_bf16 v[74:77], v[138:141], v[192:195], v[74:77]
	v_mfma_f32_16x16x32_bf16 v[126:129], v[134:137], v[166:169], v[126:129]
	v_mfma_f32_16x16x32_bf16 v[122:125], v[142:145], v[166:169], v[122:125]
	v_mfma_f32_16x16x32_bf16 v[110:113], v[134:137], v[180:183], v[110:113]
	v_mfma_f32_16x16x32_bf16 v[106:109], v[142:145], v[180:183], v[106:109]
	v_mfma_f32_16x16x32_bf16 v[94:97], v[134:137], v[188:191], v[94:97]
	v_mfma_f32_16x16x32_bf16 v[90:93], v[142:145], v[188:191], v[90:93]
	v_mfma_f32_16x16x32_bf16 v[78:81], v[134:137], v[196:199], v[78:81]
	v_mfma_f32_16x16x32_bf16 v[74:77], v[142:145], v[196:199], v[74:77]
	s_setprio 0
	s_barrier
	s_add_i32 s38, 0, 0x1c000
	s_add_i32 s39, s56, s5
	v_add_u32_e32 v175, s38, v171
	v_lshl_add_u64 v[218:219], v[218:219], 0, s[18:19]
	s_mov_b32 m0, s39
	ds_read_b128 v[200:203], v175
	ds_read_b128 v[204:207], v175 offset:1024
	ds_read_b128 v[208:211], v175 offset:2048
	ds_read_b128 v[214:217], v175 offset:3072
	global_load_lds_dwordx4 v[218:219], off
	v_lshl_add_u64 v[218:219], v[220:221], 0, s[18:19]
	s_add_i32 m0, s39, 0x2000
	s_nop 0
	global_load_lds_dwordx4 v[218:219], off
	s_barrier
	s_setprio 1
	s_waitcnt lgkmcnt(0)
	v_mfma_f32_16x16x32_bf16 v[118:121], v[200:203], v[162:165], v[118:121]
	v_mfma_f32_16x16x32_bf16 v[114:117], v[208:211], v[162:165], v[114:117]
	ds_read_b128 v[162:165], v173 offset:49152
	v_mfma_f32_16x16x32_bf16 v[102:105], v[200:203], v[176:179], v[102:105]
	v_mfma_f32_16x16x32_bf16 v[98:101], v[208:211], v[176:179], v[98:101]
	ds_read_b128 v[176:179], v173 offset:51200
	v_mfma_f32_16x16x32_bf16 v[86:89], v[200:203], v[184:187], v[86:89]
	v_mfma_f32_16x16x32_bf16 v[82:85], v[208:211], v[184:187], v[82:85]
	ds_read_b128 v[184:187], v173 offset:53248
	v_mfma_f32_16x16x32_bf16 v[70:73], v[200:203], v[192:195], v[70:73]
	v_mfma_f32_16x16x32_bf16 v[66:69], v[208:211], v[192:195], v[66:69]
	ds_read_b128 v[192:195], v173 offset:55296
	v_mfma_f32_16x16x32_bf16 v[118:121], v[204:207], v[166:169], v[118:121]
	v_mfma_f32_16x16x32_bf16 v[114:117], v[214:217], v[166:169], v[114:117]
	ds_read_b128 v[166:169], v173 offset:50176
	v_mfma_f32_16x16x32_bf16 v[102:105], v[204:207], v[180:183], v[102:105]
	v_mfma_f32_16x16x32_bf16 v[98:101], v[214:217], v[180:183], v[98:101]
	ds_read_b128 v[180:183], v173 offset:52224
	v_mfma_f32_16x16x32_bf16 v[86:89], v[204:207], v[188:191], v[86:89]
	v_mfma_f32_16x16x32_bf16 v[82:85], v[214:217], v[188:191], v[82:85]
	ds_read_b128 v[188:191], v173 offset:54272
	v_mfma_f32_16x16x32_bf16 v[70:73], v[204:207], v[196:199], v[70:73]
	v_mfma_f32_16x16x32_bf16 v[66:69], v[214:217], v[196:199], v[66:69]
	ds_read_b128 v[196:199], v173 offset:56320
	s_setprio 0
	s_mov_b32 m0, s44
	v_lshl_add_u64 v[218:219], v[222:223], 0, s[18:19]
	s_barrier
	global_load_lds_dwordx4 v[218:219], off
	v_lshl_add_u64 v[218:219], v[224:225], 0, s[18:19]
	s_mov_b32 m0, s45
	s_nop 0
	global_load_lds_dwordx4 v[218:219], off
	s_barrier
	s_setprio 1
	s_waitcnt lgkmcnt(0)
	v_mfma_f32_16x16x32_bf16 v[62:65], v[130:133], v[162:165], v[62:65]
	v_mfma_f32_16x16x32_bf16 v[58:61], v[138:141], v[162:165], v[58:61]
	v_mfma_f32_16x16x32_bf16 v[46:49], v[130:133], v[176:179], v[46:49]
	v_mfma_f32_16x16x32_bf16 v[42:45], v[138:141], v[176:179], v[42:45]
	v_mfma_f32_16x16x32_bf16 v[30:33], v[130:133], v[184:187], v[30:33]
	v_mfma_f32_16x16x32_bf16 v[26:29], v[138:141], v[184:187], v[26:29]
	v_mfma_f32_16x16x32_bf16 v[14:17], v[130:133], v[192:195], v[14:17]
	v_mfma_f32_16x16x32_bf16 v[10:13], v[138:141], v[192:195], v[10:13]
	v_mfma_f32_16x16x32_bf16 v[62:65], v[134:137], v[166:169], v[62:65]
	v_mfma_f32_16x16x32_bf16 v[58:61], v[142:145], v[166:169], v[58:61]
	v_mfma_f32_16x16x32_bf16 v[46:49], v[134:137], v[180:183], v[46:49]
	v_mfma_f32_16x16x32_bf16 v[42:45], v[142:145], v[180:183], v[42:45]
	v_mfma_f32_16x16x32_bf16 v[30:33], v[134:137], v[188:191], v[30:33]
	v_mfma_f32_16x16x32_bf16 v[26:29], v[142:145], v[188:191], v[26:29]
	v_mfma_f32_16x16x32_bf16 v[14:17], v[134:137], v[196:199], v[14:17]
	v_mfma_f32_16x16x32_bf16 v[10:13], v[142:145], v[196:199], v[10:13]
	s_setprio 0
	s_barrier
	s_add_u32 s36, s36, 0x80080
	s_addc_u32 s37, s37, 0
	s_add_i32 s38, s38, s5
	v_lshl_add_u64 v[130:131], s[36:37], 0, v[148:149]
	s_mov_b32 m0, s38
	s_nop 0
	global_load_lds_dwordx4 v[130:131], off
	v_lshl_add_u64 v[130:131], s[36:37], 0, v[152:153]
	s_add_i32 m0, s38, 0x2000
	s_nop 0
	global_load_lds_dwordx4 v[130:131], off
	s_waitcnt vmcnt(6)
	s_barrier
	s_setprio 1
	v_mfma_f32_16x16x32_bf16 v[54:57], v[200:203], v[162:165], v[54:57]
	v_mfma_f32_16x16x32_bf16 v[50:53], v[208:211], v[162:165], v[50:53]
	v_mfma_f32_16x16x32_bf16 v[38:41], v[200:203], v[176:179], v[38:41]
	v_mfma_f32_16x16x32_bf16 v[34:37], v[208:211], v[176:179], v[34:37]
	v_mfma_f32_16x16x32_bf16 v[22:25], v[200:203], v[184:187], v[22:25]
	v_mfma_f32_16x16x32_bf16 v[18:21], v[208:211], v[184:187], v[18:21]
	v_mfma_f32_16x16x32_bf16 v[6:9], v[200:203], v[192:195], v[6:9]
	v_mfma_f32_16x16x32_bf16 v[2:5], v[208:211], v[192:195], v[2:5]
	v_mfma_f32_16x16x32_bf16 v[54:57], v[204:207], v[166:169], v[54:57]
	v_mfma_f32_16x16x32_bf16 v[50:53], v[214:217], v[166:169], v[50:53]
	v_mfma_f32_16x16x32_bf16 v[38:41], v[204:207], v[180:183], v[38:41]
	v_mfma_f32_16x16x32_bf16 v[34:37], v[214:217], v[180:183], v[34:37]
	v_mfma_f32_16x16x32_bf16 v[22:25], v[204:207], v[188:191], v[22:25]
	v_mfma_f32_16x16x32_bf16 v[18:21], v[214:217], v[188:191], v[18:21]
	v_mfma_f32_16x16x32_bf16 v[6:9], v[204:207], v[196:199], v[6:9]
	v_mfma_f32_16x16x32_bf16 v[2:5], v[214:217], v[196:199], v[2:5]
	s_setprio 0
	s_add_u32 s8, s8, 0x100
	s_addc_u32 s9, s9, 0
	s_add_u32 s53, s53, 0x100
	s_addc_u32 s54, s54, 0
	s_cmp_ge_i32 s55, s1
	s_mov_b32 s36, s55
	s_barrier
	s_cbranch_scc0 .LBB0_964

.Lmy_pl2_1553:
	s_add_i32 s71, s71, 2
	s_add_u32 s30, s28, 0x100
	s_addc_u32 s31, s29, 0
	s_and_b64 s[36:37], s[34:35], exec
	s_cselect_b32 s36, 0, s30
	s_cselect_b32 s37, 0, s31
	s_add_u32 s36, s22, s36
	s_addc_u32 s37, s23, s37
	s_add_u32 s72, s69, s28
	s_addc_u32 s73, s70, s29
	s_and_b64 s[28:29], s[34:35], exec
	s_cselect_b32 s29, s67, s73
	s_cselect_b32 s28, s68, s72
	s_mov_b32 m0, s42
	v_add_u32_e32 v191, s57, v204
	v_lshl_add_u64 v[230:231], s[28:29], 0, v[188:189]
	v_add_u32_e32 v197, s57, v205
	ds_read_b128 v[214:217], v191
	ds_read_b128 v[222:225], v191 offset:2048
	ds_read_b128 v[218:221], v197
	ds_read_b128 v[226:229], v197 offset:2048
	global_load_lds_dwordx4 v[230:231], off
	v_lshl_add_u64 v[232:233], s[28:29], 0, v[186:187]
	s_mov_b32 m0, s43
	v_mfma_scale_f32_16x16x128_f8f6f4 v[174:177], v[2:9], v[26:33], 0, v211, v210 op_sel_hi:[0,0,0]
	global_load_lds_dwordx4 v[232:233], off
	s_barrier
	v_mov_b32_e32 v193, v185
	v_mov_b32_e32 v195, v185
	v_mfma_scale_f32_16x16x128_f8f6f4 v[170:173], v[10:17], v[26:33], 0, v211, v210 op_sel_hi:[0,0,0]
	v_mfma_scale_f32_16x16x128_f8f6f4 v[166:169], v[2:9], v[18:25], 0, v211, v210 op_sel_hi:[0,0,0]
	v_mfma_scale_f32_16x16x128_f8f6f4 v[162:165], v[10:17], v[18:25], 0, v211, v210 op_sel_hi:[0,0,0]
	v_mfma_scale_f32_16x16x128_f8f6f4 v[142:145], v[2:9], v[42:49], 0, v211, v210 op_sel_hi:[0,0,0]
	v_mfma_scale_f32_16x16x128_f8f6f4 v[130:133], v[10:17], v[42:49], 0, v211, v210 op_sel_hi:[0,0,0]
	v_mfma_scale_f32_16x16x128_f8f6f4 v[118:121], v[2:9], v[34:41], 0, v211, v210 op_sel_hi:[0,0,0]
	v_mfma_scale_f32_16x16x128_f8f6f4 v[114:117], v[10:17], v[34:41], 0, v211, v210 op_sel_hi:[0,0,0]
	s_setprio 1
	s_waitcnt lgkmcnt(0)
	v_mfma_scale_f32_16x16x128_f8f6f4 v[158:161], v[214:221], v[26:33], 0, v211, v210 op_sel_hi:[0,0,0]
	v_mfma_scale_f32_16x16x128_f8f6f4 v[154:157], v[222:229], v[26:33], 0, v211, v210 op_sel_hi:[0,0,0]
	ds_read_b128 v[26:29], v208 offset:18432
	ds_read_b128 v[30:33], v209 offset:18432
	v_mfma_scale_f32_16x16x128_f8f6f4 v[150:153], v[214:221], v[18:25], 0, v211, v210 op_sel_hi:[0,0,0]
	v_mfma_scale_f32_16x16x128_f8f6f4 v[146:149], v[222:229], v[18:25], 0, v211, v210 op_sel_hi:[0,0,0]
	ds_read_b128 v[18:21], v208 offset:16384
	ds_read_b128 v[22:25], v209 offset:16384
	v_mfma_scale_f32_16x16x128_f8f6f4 v[138:141], v[214:221], v[42:49], 0, v211, v210 op_sel_hi:[0,0,0]
	v_mfma_scale_f32_16x16x128_f8f6f4 v[134:137], v[222:229], v[42:49], 0, v211, v210 op_sel_hi:[0,0,0]
	ds_read_b128 v[42:45], v208 offset:22528
	ds_read_b128 v[46:49], v209 offset:22528
	v_mfma_scale_f32_16x16x128_f8f6f4 v[126:129], v[214:221], v[34:41], 0, v211, v210 op_sel_hi:[0,0,0]
	v_mfma_scale_f32_16x16x128_f8f6f4 v[122:125], v[222:229], v[34:41], 0, v211, v210 op_sel_hi:[0,0,0]
	ds_read_b128 v[34:37], v208 offset:20480
	ds_read_b128 v[38:41], v209 offset:20480
	s_setprio 0
	s_mov_b32 m0, s41
	s_barrier
	global_load_lds_dwordx4 v184, s[36:37]
	s_mov_b32 m0, s44
	v_mov_b32_e32 v191, v185
	global_load_lds_dwordx4 v190, s[36:37]
	s_barrier
	v_lshl_add_u64 v[234:235], s[36:37], 0, v[184:185]
	v_lshl_add_u64 v[236:237], s[36:37], 0, v[190:191]
	s_setprio 1
	s_waitcnt lgkmcnt(0)
	v_mfma_scale_f32_16x16x128_f8f6f4 v[110:113], v[2:9], v[18:25], 0, v211, v210 op_sel_hi:[0,0,0]
	v_mfma_scale_f32_16x16x128_f8f6f4 v[102:105], v[10:17], v[18:25], 0, v211, v210 op_sel_hi:[0,0,0]
	v_mfma_scale_f32_16x16x128_f8f6f4 v[94:97], v[2:9], v[26:33], 0, v211, v210 op_sel_hi:[0,0,0]
	v_mfma_scale_f32_16x16x128_f8f6f4 v[86:89], v[10:17], v[26:33], 0, v211, v210 op_sel_hi:[0,0,0]
	v_mfma_scale_f32_16x16x128_f8f6f4 v[78:81], v[2:9], v[34:41], 0, v211, v210 op_sel_hi:[0,0,0]
	v_mfma_scale_f32_16x16x128_f8f6f4 v[70:73], v[10:17], v[34:41], 0, v211, v210 op_sel_hi:[0,0,0]
	v_mfma_scale_f32_16x16x128_f8f6f4 v[62:65], v[2:9], v[42:49], 0, v211, v210 op_sel_hi:[0,0,0]
	v_mfma_scale_f32_16x16x128_f8f6f4 v[54:57], v[10:17], v[42:49], 0, v211, v210 op_sel_hi:[0,0,0]
	s_setprio 0
	s_barrier
	s_add_u32 s34, s28, 0x40000
	s_addc_u32 s35, s29, 0
	s_mov_b32 m0, s59
	v_lshl_add_u64 v[2:3], s[34:35], 0, v[188:189]
	global_load_lds_dwordx4 v[2:3], off
	v_lshl_add_u64 v[2:3], s[34:35], 0, v[186:187]
	s_mov_b32 m0, s60
	s_nop 0
	global_load_lds_dwordx4 v[2:3], off
	s_waitcnt vmcnt(6)
	s_barrier
	s_setprio 1
	v_mfma_scale_f32_16x16x128_f8f6f4 v[106:109], v[214:221], v[18:25], 0, v211, v210 op_sel_hi:[0,0,0]
	v_mfma_scale_f32_16x16x128_f8f6f4 v[98:101], v[222:229], v[18:25], 0, v211, v210 op_sel_hi:[0,0,0]
	ds_read_b128 v[18:21], v208 offset:32768
	ds_read_b128 v[22:25], v209 offset:32768
	v_mfma_scale_f32_16x16x128_f8f6f4 v[90:93], v[214:221], v[26:33], 0, v211, v210 op_sel_hi:[0,0,0]
	v_mfma_scale_f32_16x16x128_f8f6f4 v[82:85], v[222:229], v[26:33], 0, v211, v210 op_sel_hi:[0,0,0]
	ds_read_b128 v[26:29], v208 offset:34816
	ds_read_b128 v[30:33], v209 offset:34816
	v_mfma_scale_f32_16x16x128_f8f6f4 v[74:77], v[214:221], v[34:41], 0, v211, v210 op_sel_hi:[0,0,0]
	v_mfma_scale_f32_16x16x128_f8f6f4 v[66:69], v[222:229], v[34:41], 0, v211, v210 op_sel_hi:[0,0,0]
	ds_read_b128 v[34:37], v208 offset:36864
	ds_read_b128 v[38:41], v209 offset:36864
	v_mfma_scale_f32_16x16x128_f8f6f4 v[58:61], v[214:221], v[42:49], 0, v211, v210 op_sel_hi:[0,0,0]
	v_mfma_scale_f32_16x16x128_f8f6f4 v[50:53], v[222:229], v[42:49], 0, v211, v210 op_sel_hi:[0,0,0]
	ds_read_b128 v[42:45], v208 offset:38912
	ds_read_b128 v[46:49], v209 offset:38912
	s_setprio 0
	v_add_u32_e32 v6, s61, v204
	v_add_u32_e32 v14, s61, v205
	s_barrier
	ds_read_b128 v[2:5], v6
	ds_read_b128 v[10:13], v6 offset:2048
	ds_read_b128 v[6:9], v14
	ds_read_b128 v[14:17], v14 offset:2048
	s_mov_b32 m0, s45
	v_lshl_add_u64 v[214:215], s[36:37], 0, v[192:193]
	global_load_lds_dwordx4 v[214:215], off
	v_lshl_add_u64 v[214:215], s[36:37], 0, v[194:195]
	s_mov_b32 m0, s46
	s_nop 0
	global_load_lds_dwordx4 v[214:215], off
	s_waitcnt lgkmcnt(8)
	s_barrier
	s_setprio 1
	s_waitcnt lgkmcnt(0)
	v_mfma_scale_f32_16x16x128_f8f6f4 v[174:177], v[2:9], v[18:25], v[174:177], v211, v210 op_sel_hi:[0,0,0]
	v_mfma_scale_f32_16x16x128_f8f6f4 v[170:173], v[10:17], v[18:25], v[170:173], v211, v210 op_sel_hi:[0,0,0]
	v_mfma_scale_f32_16x16x128_f8f6f4 v[166:169], v[2:9], v[26:33], v[166:169], v211, v210 op_sel_hi:[0,0,0]
	v_mfma_scale_f32_16x16x128_f8f6f4 v[162:165], v[10:17], v[26:33], v[162:165], v211, v210 op_sel_hi:[0,0,0]
	v_mfma_scale_f32_16x16x128_f8f6f4 v[142:145], v[2:9], v[34:41], v[142:145], v211, v210 op_sel_hi:[0,0,0]
	v_mfma_scale_f32_16x16x128_f8f6f4 v[130:133], v[10:17], v[34:41], v[130:133], v211, v210 op_sel_hi:[0,0,0]
	v_mfma_scale_f32_16x16x128_f8f6f4 v[118:121], v[2:9], v[42:49], v[118:121], v211, v210 op_sel_hi:[0,0,0]
	v_mfma_scale_f32_16x16x128_f8f6f4 v[114:117], v[10:17], v[42:49], v[114:117], v211, v210 op_sel_hi:[0,0,0]
	s_setprio 0
	s_barrier
	s_mov_b32 m0, s63
	v_add_u32_e32 v191, s62, v204
	v_lshl_add_u64 v[230:231], v[230:231], 0, s[12:13]
	v_add_u32_e32 v193, s62, v205
	ds_read_b128 v[214:217], v191
	ds_read_b128 v[222:225], v191 offset:2048
	ds_read_b128 v[218:221], v193
	ds_read_b128 v[226:229], v193 offset:2048
	global_load_lds_dwordx4 v[230:231], off
	v_lshl_add_u64 v[230:231], v[232:233], 0, s[12:13]
	s_add_i32 m0, s63, 0x2000
	s_nop 0
	global_load_lds_dwordx4 v[230:231], off
	s_barrier
	s_setprio 1
	s_waitcnt lgkmcnt(0)
	v_mfma_scale_f32_16x16x128_f8f6f4 v[158:161], v[214:221], v[18:25], v[158:161], v211, v210 op_sel_hi:[0,0,0]
	v_mfma_scale_f32_16x16x128_f8f6f4 v[154:157], v[222:229], v[18:25], v[154:157], v211, v210 op_sel_hi:[0,0,0]
	ds_read_b128 v[18:21], v208 offset:49152
	ds_read_b128 v[22:25], v209 offset:49152
	v_mfma_scale_f32_16x16x128_f8f6f4 v[150:153], v[214:221], v[26:33], v[150:153], v211, v210 op_sel_hi:[0,0,0]
	v_mfma_scale_f32_16x16x128_f8f6f4 v[146:149], v[222:229], v[26:33], v[146:149], v211, v210 op_sel_hi:[0,0,0]
	ds_read_b128 v[26:29], v208 offset:51200
	ds_read_b128 v[30:33], v209 offset:51200
	v_mfma_scale_f32_16x16x128_f8f6f4 v[138:141], v[214:221], v[34:41], v[138:141], v211, v210 op_sel_hi:[0,0,0]
	v_mfma_scale_f32_16x16x128_f8f6f4 v[134:137], v[222:229], v[34:41], v[134:137], v211, v210 op_sel_hi:[0,0,0]
	ds_read_b128 v[34:37], v208 offset:53248
	ds_read_b128 v[38:41], v209 offset:53248
	v_mfma_scale_f32_16x16x128_f8f6f4 v[126:129], v[214:221], v[42:49], v[126:129], v211, v210 op_sel_hi:[0,0,0]
	v_mfma_scale_f32_16x16x128_f8f6f4 v[122:125], v[222:229], v[42:49], v[122:125], v211, v210 op_sel_hi:[0,0,0]
	ds_read_b128 v[42:45], v208 offset:55296
	ds_read_b128 v[46:49], v209 offset:55296
	s_setprio 0
	s_mov_b32 m0, s49
	v_lshl_add_u64 v[230:231], v[234:235], 0, s[12:13]
	s_barrier
	global_load_lds_dwordx4 v[230:231], off
	v_lshl_add_u64 v[230:231], v[236:237], 0, s[12:13]
	s_mov_b32 m0, s50
	s_nop 0
	global_load_lds_dwordx4 v[230:231], off
	s_barrier
	s_setprio 1
	s_waitcnt lgkmcnt(0)
	v_mfma_scale_f32_16x16x128_f8f6f4 v[110:113], v[2:9], v[18:25], v[110:113], v211, v210 op_sel_hi:[0,0,0]
	v_mfma_scale_f32_16x16x128_f8f6f4 v[102:105], v[10:17], v[18:25], v[102:105], v211, v210 op_sel_hi:[0,0,0]
	v_mfma_scale_f32_16x16x128_f8f6f4 v[94:97], v[2:9], v[26:33], v[94:97], v211, v210 op_sel_hi:[0,0,0]
	v_mfma_scale_f32_16x16x128_f8f6f4 v[86:89], v[10:17], v[26:33], v[86:89], v211, v210 op_sel_hi:[0,0,0]
	v_mfma_scale_f32_16x16x128_f8f6f4 v[78:81], v[2:9], v[34:41], v[78:81], v211, v210 op_sel_hi:[0,0,0]
	v_mfma_scale_f32_16x16x128_f8f6f4 v[70:73], v[10:17], v[34:41], v[70:73], v211, v210 op_sel_hi:[0,0,0]
	v_mfma_scale_f32_16x16x128_f8f6f4 v[62:65], v[2:9], v[42:49], v[62:65], v211, v210 op_sel_hi:[0,0,0]
	v_mfma_scale_f32_16x16x128_f8f6f4 v[54:57], v[10:17], v[42:49], v[54:57], v211, v210 op_sel_hi:[0,0,0]
	s_setprio 0
	s_barrier
	s_add_u32 s28, s28, 0x40080
	s_addc_u32 s29, s29, 0
	s_add_i32 s34, s62, s40
	v_lshl_add_u64 v[2:3], s[28:29], 0, v[188:189]
	s_mov_b32 m0, s34
	s_nop 0
	global_load_lds_dwordx4 v[2:3], off
	v_lshl_add_u64 v[2:3], s[28:29], 0, v[186:187]
	s_add_i32 m0, s34, 0x2000
	s_nop 0
	global_load_lds_dwordx4 v[2:3], off
	s_waitcnt vmcnt(6)
	s_barrier
	s_setprio 1
	v_mfma_scale_f32_16x16x128_f8f6f4 v[106:109], v[214:221], v[18:25], v[106:109], v211, v210 op_sel_hi:[0,0,0]
	v_mfma_scale_f32_16x16x128_f8f6f4 v[98:101], v[222:229], v[18:25], v[98:101], v211, v210 op_sel_hi:[0,0,0]
	v_mfma_scale_f32_16x16x128_f8f6f4 v[90:93], v[214:221], v[26:33], v[90:93], v211, v210 op_sel_hi:[0,0,0]
	v_mfma_scale_f32_16x16x128_f8f6f4 v[82:85], v[222:229], v[26:33], v[82:85], v211, v210 op_sel_hi:[0,0,0]
	v_mfma_scale_f32_16x16x128_f8f6f4 v[74:77], v[214:221], v[34:41], v[74:77], v211, v210 op_sel_hi:[0,0,0]
	v_mfma_scale_f32_16x16x128_f8f6f4 v[66:69], v[222:229], v[34:41], v[66:69], v211, v210 op_sel_hi:[0,0,0]
	v_mfma_scale_f32_16x16x128_f8f6f4 v[58:61], v[214:221], v[42:49], v[58:61], v211, v210 op_sel_hi:[0,0,0]
	v_mfma_scale_f32_16x16x128_f8f6f4 v[50:53], v[222:229], v[42:49], v[50:53], v211, v210 op_sel_hi:[0,0,0]
	s_setprio 0
	s_cmp_ge_i32 s71, s39
	s_barrier
	s_cbranch_scc1 .LBB0_1546
	s_mov_b64 s[28:29], s[30:31]
	s_branch .LBB0_1551

.LBB0_1553:
	s_add_i32 s71, s71, 2
	s_add_u32 s30, s28, 0x100
	s_addc_u32 s31, s29, 0
	s_and_b64 s[36:37], s[34:35], exec
	s_cselect_b32 s36, 0, s30
	s_cselect_b32 s37, 0, s31
	s_add_u32 s36, s22, s36
	s_addc_u32 s37, s23, s37
	s_add_u32 s72, s69, s28
	s_addc_u32 s73, s70, s29
	s_and_b64 s[28:29], s[34:35], exec
	s_cselect_b32 s29, s67, s73
	s_cselect_b32 s28, s68, s72
	s_mov_b32 m0, s42
	v_add_u32_e32 v191, s57, v204
	v_lshl_add_u64 v[230:231], s[28:29], 0, v[188:189]
	v_add_u32_e32 v197, s57, v205
	ds_read_b128 v[214:217], v191
	ds_read_b128 v[222:225], v191 offset:2048
	ds_read_b128 v[218:221], v197
	ds_read_b128 v[226:229], v197 offset:2048
	global_load_lds_dwordx4 v[230:231], off
	v_lshl_add_u64 v[232:233], s[28:29], 0, v[186:187]
	s_mov_b32 m0, s43
	v_mfma_scale_f32_16x16x128_f8f6f4 v[174:177], v[2:9], v[26:33], v[174:177], v211, v210 op_sel_hi:[0,0,0]
	global_load_lds_dwordx4 v[232:233], off
	s_barrier
	v_mov_b32_e32 v193, v185
	v_mov_b32_e32 v195, v185
	v_mfma_scale_f32_16x16x128_f8f6f4 v[170:173], v[10:17], v[26:33], v[170:173], v211, v210 op_sel_hi:[0,0,0]
	v_mfma_scale_f32_16x16x128_f8f6f4 v[166:169], v[2:9], v[18:25], v[166:169], v211, v210 op_sel_hi:[0,0,0]
	v_mfma_scale_f32_16x16x128_f8f6f4 v[162:165], v[10:17], v[18:25], v[162:165], v211, v210 op_sel_hi:[0,0,0]
	v_mfma_scale_f32_16x16x128_f8f6f4 v[142:145], v[2:9], v[42:49], v[142:145], v211, v210 op_sel_hi:[0,0,0]
	v_mfma_scale_f32_16x16x128_f8f6f4 v[130:133], v[10:17], v[42:49], v[130:133], v211, v210 op_sel_hi:[0,0,0]
	v_mfma_scale_f32_16x16x128_f8f6f4 v[118:121], v[2:9], v[34:41], v[118:121], v211, v210 op_sel_hi:[0,0,0]
	v_mfma_scale_f32_16x16x128_f8f6f4 v[114:117], v[10:17], v[34:41], v[114:117], v211, v210 op_sel_hi:[0,0,0]
	s_setprio 1
	s_waitcnt lgkmcnt(0)
	v_mfma_scale_f32_16x16x128_f8f6f4 v[158:161], v[214:221], v[26:33], v[158:161], v211, v210 op_sel_hi:[0,0,0]
	v_mfma_scale_f32_16x16x128_f8f6f4 v[154:157], v[222:229], v[26:33], v[154:157], v211, v210 op_sel_hi:[0,0,0]
	ds_read_b128 v[26:29], v208 offset:18432
	ds_read_b128 v[30:33], v209 offset:18432
	v_mfma_scale_f32_16x16x128_f8f6f4 v[150:153], v[214:221], v[18:25], v[150:153], v211, v210 op_sel_hi:[0,0,0]
	v_mfma_scale_f32_16x16x128_f8f6f4 v[146:149], v[222:229], v[18:25], v[146:149], v211, v210 op_sel_hi:[0,0,0]
	ds_read_b128 v[18:21], v208 offset:16384
	ds_read_b128 v[22:25], v209 offset:16384
	v_mfma_scale_f32_16x16x128_f8f6f4 v[138:141], v[214:221], v[42:49], v[138:141], v211, v210 op_sel_hi:[0,0,0]
	v_mfma_scale_f32_16x16x128_f8f6f4 v[134:137], v[222:229], v[42:49], v[134:137], v211, v210 op_sel_hi:[0,0,0]
	ds_read_b128 v[42:45], v208 offset:22528
	ds_read_b128 v[46:49], v209 offset:22528
	v_mfma_scale_f32_16x16x128_f8f6f4 v[126:129], v[214:221], v[34:41], v[126:129], v211, v210 op_sel_hi:[0,0,0]
	v_mfma_scale_f32_16x16x128_f8f6f4 v[122:125], v[222:229], v[34:41], v[122:125], v211, v210 op_sel_hi:[0,0,0]
	ds_read_b128 v[34:37], v208 offset:20480
	ds_read_b128 v[38:41], v209 offset:20480
	s_setprio 0
	s_mov_b32 m0, s41
	s_barrier
	global_load_lds_dwordx4 v184, s[36:37]
	s_mov_b32 m0, s44
	v_mov_b32_e32 v191, v185
	global_load_lds_dwordx4 v190, s[36:37]
	s_barrier
	v_lshl_add_u64 v[234:235], s[36:37], 0, v[184:185]
	v_lshl_add_u64 v[236:237], s[36:37], 0, v[190:191]
	s_setprio 1
	s_waitcnt lgkmcnt(0)
	v_mfma_scale_f32_16x16x128_f8f6f4 v[110:113], v[2:9], v[18:25], v[110:113], v211, v210 op_sel_hi:[0,0,0]
	v_mfma_scale_f32_16x16x128_f8f6f4 v[102:105], v[10:17], v[18:25], v[102:105], v211, v210 op_sel_hi:[0,0,0]
	v_mfma_scale_f32_16x16x128_f8f6f4 v[94:97], v[2:9], v[26:33], v[94:97], v211, v210 op_sel_hi:[0,0,0]
	v_mfma_scale_f32_16x16x128_f8f6f4 v[86:89], v[10:17], v[26:33], v[86:89], v211, v210 op_sel_hi:[0,0,0]
	v_mfma_scale_f32_16x16x128_f8f6f4 v[78:81], v[2:9], v[34:41], v[78:81], v211, v210 op_sel_hi:[0,0,0]
	v_mfma_scale_f32_16x16x128_f8f6f4 v[70:73], v[10:17], v[34:41], v[70:73], v211, v210 op_sel_hi:[0,0,0]
	v_mfma_scale_f32_16x16x128_f8f6f4 v[62:65], v[2:9], v[42:49], v[62:65], v211, v210 op_sel_hi:[0,0,0]
	v_mfma_scale_f32_16x16x128_f8f6f4 v[54:57], v[10:17], v[42:49], v[54:57], v211, v210 op_sel_hi:[0,0,0]
	s_setprio 0
	s_barrier
	s_add_u32 s34, s28, 0x40000
	s_addc_u32 s35, s29, 0
	s_mov_b32 m0, s59
	v_lshl_add_u64 v[2:3], s[34:35], 0, v[188:189]
	global_load_lds_dwordx4 v[2:3], off
	v_lshl_add_u64 v[2:3], s[34:35], 0, v[186:187]
	s_mov_b32 m0, s60
	s_nop 0
	global_load_lds_dwordx4 v[2:3], off
	s_waitcnt vmcnt(6)
	s_barrier
	s_setprio 1
	v_mfma_scale_f32_16x16x128_f8f6f4 v[106:109], v[214:221], v[18:25], v[106:109], v211, v210 op_sel_hi:[0,0,0]
	v_mfma_scale_f32_16x16x128_f8f6f4 v[98:101], v[222:229], v[18:25], v[98:101], v211, v210 op_sel_hi:[0,0,0]
	ds_read_b128 v[18:21], v208 offset:32768
	ds_read_b128 v[22:25], v209 offset:32768
	v_mfma_scale_f32_16x16x128_f8f6f4 v[90:93], v[214:221], v[26:33], v[90:93], v211, v210 op_sel_hi:[0,0,0]
	v_mfma_scale_f32_16x16x128_f8f6f4 v[82:85], v[222:229], v[26:33], v[82:85], v211, v210 op_sel_hi:[0,0,0]
	ds_read_b128 v[26:29], v208 offset:34816
	ds_read_b128 v[30:33], v209 offset:34816
	v_mfma_scale_f32_16x16x128_f8f6f4 v[74:77], v[214:221], v[34:41], v[74:77], v211, v210 op_sel_hi:[0,0,0]
	v_mfma_scale_f32_16x16x128_f8f6f4 v[66:69], v[222:229], v[34:41], v[66:69], v211, v210 op_sel_hi:[0,0,0]
	ds_read_b128 v[34:37], v208 offset:36864
	ds_read_b128 v[38:41], v209 offset:36864
	v_mfma_scale_f32_16x16x128_f8f6f4 v[58:61], v[214:221], v[42:49], v[58:61], v211, v210 op_sel_hi:[0,0,0]
	v_mfma_scale_f32_16x16x128_f8f6f4 v[50:53], v[222:229], v[42:49], v[50:53], v211, v210 op_sel_hi:[0,0,0]
	ds_read_b128 v[42:45], v208 offset:38912
	ds_read_b128 v[46:49], v209 offset:38912
	s_setprio 0
	v_add_u32_e32 v6, s61, v204
	v_add_u32_e32 v14, s61, v205
	s_barrier
	ds_read_b128 v[2:5], v6
	ds_read_b128 v[10:13], v6 offset:2048
	ds_read_b128 v[6:9], v14
	ds_read_b128 v[14:17], v14 offset:2048
	s_mov_b32 m0, s45
	v_lshl_add_u64 v[214:215], s[36:37], 0, v[192:193]
	global_load_lds_dwordx4 v[214:215], off
	v_lshl_add_u64 v[214:215], s[36:37], 0, v[194:195]
	s_mov_b32 m0, s46
	s_nop 0
	global_load_lds_dwordx4 v[214:215], off
	s_waitcnt lgkmcnt(8)
	s_barrier
	s_setprio 1
	s_waitcnt lgkmcnt(0)
	v_mfma_scale_f32_16x16x128_f8f6f4 v[174:177], v[2:9], v[18:25], v[174:177], v211, v210 op_sel_hi:[0,0,0]
	v_mfma_scale_f32_16x16x128_f8f6f4 v[170:173], v[10:17], v[18:25], v[170:173], v211, v210 op_sel_hi:[0,0,0]
	v_mfma_scale_f32_16x16x128_f8f6f4 v[166:169], v[2:9], v[26:33], v[166:169], v211, v210 op_sel_hi:[0,0,0]
	v_mfma_scale_f32_16x16x128_f8f6f4 v[162:165], v[10:17], v[26:33], v[162:165], v211, v210 op_sel_hi:[0,0,0]
	v_mfma_scale_f32_16x16x128_f8f6f4 v[142:145], v[2:9], v[34:41], v[142:145], v211, v210 op_sel_hi:[0,0,0]
	v_mfma_scale_f32_16x16x128_f8f6f4 v[130:133], v[10:17], v[34:41], v[130:133], v211, v210 op_sel_hi:[0,0,0]
	v_mfma_scale_f32_16x16x128_f8f6f4 v[118:121], v[2:9], v[42:49], v[118:121], v211, v210 op_sel_hi:[0,0,0]
	v_mfma_scale_f32_16x16x128_f8f6f4 v[114:117], v[10:17], v[42:49], v[114:117], v211, v210 op_sel_hi:[0,0,0]
	s_setprio 0
	s_barrier
	s_mov_b32 m0, s63
	v_add_u32_e32 v191, s62, v204
	v_lshl_add_u64 v[230:231], v[230:231], 0, s[12:13]
	v_add_u32_e32 v193, s62, v205
	ds_read_b128 v[214:217], v191
	ds_read_b128 v[222:225], v191 offset:2048
	ds_read_b128 v[218:221], v193
	ds_read_b128 v[226:229], v193 offset:2048
	global_load_lds_dwordx4 v[230:231], off
	v_lshl_add_u64 v[230:231], v[232:233], 0, s[12:13]
	s_add_i32 m0, s63, 0x2000
	s_nop 0
	global_load_lds_dwordx4 v[230:231], off
	s_barrier
	s_setprio 1
	s_waitcnt lgkmcnt(0)
	v_mfma_scale_f32_16x16x128_f8f6f4 v[158:161], v[214:221], v[18:25], v[158:161], v211, v210 op_sel_hi:[0,0,0]
	v_mfma_scale_f32_16x16x128_f8f6f4 v[154:157], v[222:229], v[18:25], v[154:157], v211, v210 op_sel_hi:[0,0,0]
	ds_read_b128 v[18:21], v208 offset:49152
	ds_read_b128 v[22:25], v209 offset:49152
	v_mfma_scale_f32_16x16x128_f8f6f4 v[150:153], v[214:221], v[26:33], v[150:153], v211, v210 op_sel_hi:[0,0,0]
	v_mfma_scale_f32_16x16x128_f8f6f4 v[146:149], v[222:229], v[26:33], v[146:149], v211, v210 op_sel_hi:[0,0,0]
	ds_read_b128 v[26:29], v208 offset:51200
	ds_read_b128 v[30:33], v209 offset:51200
	v_mfma_scale_f32_16x16x128_f8f6f4 v[138:141], v[214:221], v[34:41], v[138:141], v211, v210 op_sel_hi:[0,0,0]
	v_mfma_scale_f32_16x16x128_f8f6f4 v[134:137], v[222:229], v[34:41], v[134:137], v211, v210 op_sel_hi:[0,0,0]
	ds_read_b128 v[34:37], v208 offset:53248
	ds_read_b128 v[38:41], v209 offset:53248
	v_mfma_scale_f32_16x16x128_f8f6f4 v[126:129], v[214:221], v[42:49], v[126:129], v211, v210 op_sel_hi:[0,0,0]
	v_mfma_scale_f32_16x16x128_f8f6f4 v[122:125], v[222:229], v[42:49], v[122:125], v211, v210 op_sel_hi:[0,0,0]
	ds_read_b128 v[42:45], v208 offset:55296
	ds_read_b128 v[46:49], v209 offset:55296
	s_setprio 0
	s_mov_b32 m0, s49
	v_lshl_add_u64 v[230:231], v[234:235], 0, s[12:13]
	s_barrier
	global_load_lds_dwordx4 v[230:231], off
	v_lshl_add_u64 v[230:231], v[236:237], 0, s[12:13]
	s_mov_b32 m0, s50
	s_nop 0
	global_load_lds_dwordx4 v[230:231], off
	s_barrier
	s_setprio 1
	s_waitcnt lgkmcnt(0)
	v_mfma_scale_f32_16x16x128_f8f6f4 v[110:113], v[2:9], v[18:25], v[110:113], v211, v210 op_sel_hi:[0,0,0]
	v_mfma_scale_f32_16x16x128_f8f6f4 v[102:105], v[10:17], v[18:25], v[102:105], v211, v210 op_sel_hi:[0,0,0]
	v_mfma_scale_f32_16x16x128_f8f6f4 v[94:97], v[2:9], v[26:33], v[94:97], v211, v210 op_sel_hi:[0,0,0]
	v_mfma_scale_f32_16x16x128_f8f6f4 v[86:89], v[10:17], v[26:33], v[86:89], v211, v210 op_sel_hi:[0,0,0]
	v_mfma_scale_f32_16x16x128_f8f6f4 v[78:81], v[2:9], v[34:41], v[78:81], v211, v210 op_sel_hi:[0,0,0]
	v_mfma_scale_f32_16x16x128_f8f6f4 v[70:73], v[10:17], v[34:41], v[70:73], v211, v210 op_sel_hi:[0,0,0]
	v_mfma_scale_f32_16x16x128_f8f6f4 v[62:65], v[2:9], v[42:49], v[62:65], v211, v210 op_sel_hi:[0,0,0]
	v_mfma_scale_f32_16x16x128_f8f6f4 v[54:57], v[10:17], v[42:49], v[54:57], v211, v210 op_sel_hi:[0,0,0]
	s_setprio 0
	s_barrier
	s_add_u32 s28, s28, 0x40080
	s_addc_u32 s29, s29, 0
	s_add_i32 s34, s62, s40
	v_lshl_add_u64 v[2:3], s[28:29], 0, v[188:189]
	s_mov_b32 m0, s34
	s_nop 0
	global_load_lds_dwordx4 v[2:3], off
	v_lshl_add_u64 v[2:3], s[28:29], 0, v[186:187]
	s_add_i32 m0, s34, 0x2000
	s_nop 0
	global_load_lds_dwordx4 v[2:3], off
	s_waitcnt vmcnt(6)
	s_barrier
	s_setprio 1
	v_mfma_scale_f32_16x16x128_f8f6f4 v[106:109], v[214:221], v[18:25], v[106:109], v211, v210 op_sel_hi:[0,0,0]
	v_mfma_scale_f32_16x16x128_f8f6f4 v[98:101], v[222:229], v[18:25], v[98:101], v211, v210 op_sel_hi:[0,0,0]
	v_mfma_scale_f32_16x16x128_f8f6f4 v[90:93], v[214:221], v[26:33], v[90:93], v211, v210 op_sel_hi:[0,0,0]
	v_mfma_scale_f32_16x16x128_f8f6f4 v[82:85], v[222:229], v[26:33], v[82:85], v211, v210 op_sel_hi:[0,0,0]
	v_mfma_scale_f32_16x16x128_f8f6f4 v[74:77], v[214:221], v[34:41], v[74:77], v211, v210 op_sel_hi:[0,0,0]
	v_mfma_scale_f32_16x16x128_f8f6f4 v[66:69], v[222:229], v[34:41], v[66:69], v211, v210 op_sel_hi:[0,0,0]
	v_mfma_scale_f32_16x16x128_f8f6f4 v[58:61], v[214:221], v[42:49], v[58:61], v211, v210 op_sel_hi:[0,0,0]
	v_mfma_scale_f32_16x16x128_f8f6f4 v[50:53], v[222:229], v[42:49], v[50:53], v211, v210 op_sel_hi:[0,0,0]
	s_setprio 0
	s_cmp_ge_i32 s71, s39
	s_barrier
	s_cbranch_scc1 .LBB0_1546
	s_mov_b64 s[28:29], s[30:31]
	s_branch .LBB0_1551

.Lmy_pl3_1675:
	s_add_i32 s59, s59, 2
	s_add_u32 s24, s22, 0x100
	s_addc_u32 s25, s23, 0
	s_and_b64 s[28:29], s[26:27], exec
	s_cselect_b32 s28, 0, s24
	s_cselect_b32 s29, 0, s25
	s_add_u32 s28, s12, s28
	s_addc_u32 s29, s13, s29
	s_add_u32 s60, s57, s22
	s_addc_u32 s61, s58, s23
	s_and_b64 s[22:23], s[26:27], exec
	s_cselect_b32 s23, s55, s61
	s_cselect_b32 s22, s56, s60
	s_mov_b32 m0, s5
	s_waitcnt lgkmcnt(0)
	v_mfma_scale_f32_16x16x128_f8f6f4 v[222:225], v[2:9], v[42:49], 0, v209, v208 op_sel_hi:[0,0,0]
	v_lshl_add_u64 v[238:239], s[22:23], 0, v[188:189]
	v_add_u32_e32 v191, s46, v203
	v_lshl_add_u64 v[240:241], s[22:23], 0, v[186:187]
	v_mov_b32_e32 v193, v185
	v_mov_b32_e32 v195, v185
	s_nop 1
	v_add_u32_e32 v142, s46, v202
	v_mfma_scale_f32_16x16x128_f8f6f4 v[226:229], v[10:17], v[42:49], 0, v209, v208 op_sel_hi:[0,0,0]
	s_nop 6
	ds_read_b128 v[138:141], v142
	ds_read_b128 v[214:217], v142 offset:2048
	ds_read_b128 v[142:145], v191
	ds_read_b128 v[218:221], v191 offset:2048
	global_load_lds_dwordx4 v[238:239], off
	s_mov_b32 m0, s31
	s_nop 0
	global_load_lds_dwordx4 v[240:241], off
	v_mfma_scale_f32_16x16x128_f8f6f4 v[174:177], v[2:9], v[26:33], 0, v209, v208 op_sel_hi:[0,0,0]
	s_barrier
	v_mfma_scale_f32_16x16x128_f8f6f4 v[170:173], v[10:17], v[26:33], 0, v209, v208 op_sel_hi:[0,0,0]
	v_mfma_scale_f32_16x16x128_f8f6f4 v[166:169], v[2:9], v[18:25], 0, v209, v208 op_sel_hi:[0,0,0]
	v_mfma_scale_f32_16x16x128_f8f6f4 v[162:165], v[10:17], v[18:25], 0, v209, v208 op_sel_hi:[0,0,0]
	v_mfma_scale_f32_16x16x128_f8f6f4 v[134:137], v[2:9], v[34:41], 0, v209, v208 op_sel_hi:[0,0,0]
	v_mfma_scale_f32_16x16x128_f8f6f4 v[122:125], v[10:17], v[34:41], 0, v209, v208 op_sel_hi:[0,0,0]
	s_setprio 1
	s_waitcnt lgkmcnt(0)
	v_mfma_scale_f32_16x16x128_f8f6f4 v[158:161], v[138:145], v[26:33], 0, v209, v208 op_sel_hi:[0,0,0]
	v_mfma_scale_f32_16x16x128_f8f6f4 v[154:157], v[214:221], v[26:33], 0, v209, v208 op_sel_hi:[0,0,0]
	ds_read_b128 v[26:29], v206 offset:18432
	ds_read_b128 v[30:33], v207 offset:18432
	v_mfma_scale_f32_16x16x128_f8f6f4 v[150:153], v[138:145], v[18:25], 0, v209, v208 op_sel_hi:[0,0,0]
	v_mfma_scale_f32_16x16x128_f8f6f4 v[146:149], v[214:221], v[18:25], 0, v209, v208 op_sel_hi:[0,0,0]
	ds_read_b128 v[18:21], v206 offset:16384
	ds_read_b128 v[22:25], v207 offset:16384
	v_mfma_scale_f32_16x16x128_f8f6f4 v[130:133], v[138:145], v[42:49], 0, v209, v208 op_sel_hi:[0,0,0]
	v_mfma_scale_f32_16x16x128_f8f6f4 v[126:129], v[214:221], v[42:49], 0, v209, v208 op_sel_hi:[0,0,0]
	ds_read_b128 v[42:45], v206 offset:22528
	ds_read_b128 v[46:49], v207 offset:22528
	v_mfma_scale_f32_16x16x128_f8f6f4 v[118:121], v[138:145], v[34:41], 0, v209, v208 op_sel_hi:[0,0,0]
	v_mfma_scale_f32_16x16x128_f8f6f4 v[114:117], v[214:221], v[34:41], 0, v209, v208 op_sel_hi:[0,0,0]
	ds_read_b128 v[34:37], v206 offset:20480
	ds_read_b128 v[38:41], v207 offset:20480
	s_setprio 0
	s_mov_b32 m0, s4
	s_barrier
	global_load_lds_dwordx4 v184, s[28:29]
	s_mov_b32 m0, s33
	v_mov_b32_e32 v191, v185
	global_load_lds_dwordx4 v190, s[28:29]
	s_barrier
	v_lshl_add_u64 v[242:243], s[28:29], 0, v[184:185]
	v_lshl_add_u64 v[244:245], s[28:29], 0, v[190:191]
	s_setprio 1
	s_waitcnt lgkmcnt(0)
	v_mfma_scale_f32_16x16x128_f8f6f4 v[110:113], v[2:9], v[18:25], 0, v209, v208 op_sel_hi:[0,0,0]
	v_mfma_scale_f32_16x16x128_f8f6f4 v[106:109], v[10:17], v[18:25], 0, v209, v208 op_sel_hi:[0,0,0]
	v_mfma_scale_f32_16x16x128_f8f6f4 v[102:105], v[2:9], v[26:33], 0, v209, v208 op_sel_hi:[0,0,0]
	v_mfma_scale_f32_16x16x128_f8f6f4 v[98:101], v[10:17], v[26:33], 0, v209, v208 op_sel_hi:[0,0,0]
	v_mfma_scale_f32_16x16x128_f8f6f4 v[78:81], v[2:9], v[34:41], 0, v209, v208 op_sel_hi:[0,0,0]
	v_mfma_scale_f32_16x16x128_f8f6f4 v[74:77], v[10:17], v[34:41], 0, v209, v208 op_sel_hi:[0,0,0]
	v_mfma_scale_f32_16x16x128_f8f6f4 v[70:73], v[2:9], v[42:49], 0, v209, v208 op_sel_hi:[0,0,0]
	v_mfma_scale_f32_16x16x128_f8f6f4 v[66:69], v[10:17], v[42:49], 0, v209, v208 op_sel_hi:[0,0,0]
	s_setprio 0
	s_barrier
	s_add_u32 s26, s22, 0x10000
	s_addc_u32 s27, s23, 0
	s_mov_b32 m0, s48
	v_lshl_add_u64 v[2:3], s[26:27], 0, v[188:189]
	global_load_lds_dwordx4 v[2:3], off
	v_lshl_add_u64 v[2:3], s[26:27], 0, v[186:187]
	s_mov_b32 m0, s49
	s_nop 0
	global_load_lds_dwordx4 v[2:3], off
	s_waitcnt vmcnt(6)
	s_barrier
	s_setprio 1
	v_mfma_scale_f32_16x16x128_f8f6f4 v[94:97], v[138:145], v[18:25], 0, v209, v208 op_sel_hi:[0,0,0]
	v_mfma_scale_f32_16x16x128_f8f6f4 v[90:93], v[214:221], v[18:25], 0, v209, v208 op_sel_hi:[0,0,0]
	ds_read_b128 v[18:21], v206 offset:32768
	ds_read_b128 v[22:25], v207 offset:32768
	v_mfma_scale_f32_16x16x128_f8f6f4 v[86:89], v[138:145], v[26:33], 0, v209, v208 op_sel_hi:[0,0,0]
	v_mfma_scale_f32_16x16x128_f8f6f4 v[82:85], v[214:221], v[26:33], 0, v209, v208 op_sel_hi:[0,0,0]
	ds_read_b128 v[26:29], v206 offset:34816
	ds_read_b128 v[30:33], v207 offset:34816
	v_mfma_scale_f32_16x16x128_f8f6f4 v[62:65], v[138:145], v[34:41], 0, v209, v208 op_sel_hi:[0,0,0]
	v_mfma_scale_f32_16x16x128_f8f6f4 v[58:61], v[214:221], v[34:41], 0, v209, v208 op_sel_hi:[0,0,0]
	ds_read_b128 v[34:37], v206 offset:36864
	ds_read_b128 v[38:41], v207 offset:36864
	v_mfma_scale_f32_16x16x128_f8f6f4 v[230:233], v[138:145], v[42:49], 0, v209, v208 op_sel_hi:[0,0,0]
	v_mfma_scale_f32_16x16x128_f8f6f4 v[234:237], v[214:221], v[42:49], 0, v209, v208 op_sel_hi:[0,0,0]
	ds_read_b128 v[42:45], v206 offset:38912
	ds_read_b128 v[46:49], v207 offset:38912
	s_setprio 0
	v_add_u32_e32 v6, s50, v202
	v_add_u32_e32 v14, s50, v203
	s_barrier
	ds_read_b128 v[2:5], v6
	ds_read_b128 v[10:13], v6 offset:2048
	ds_read_b128 v[6:9], v14
	ds_read_b128 v[14:17], v14 offset:2048
	s_mov_b32 m0, s34
	v_lshl_add_u64 v[50:51], s[28:29], 0, v[192:193]
	global_load_lds_dwordx4 v[50:51], off
	v_lshl_add_u64 v[50:51], s[28:29], 0, v[194:195]
	s_mov_b32 m0, s35
	s_nop 0
	global_load_lds_dwordx4 v[50:51], off
	s_waitcnt lgkmcnt(8)
	s_barrier
	s_setprio 1
	s_waitcnt lgkmcnt(0)
	v_mfma_scale_f32_16x16x128_f8f6f4 v[174:177], v[2:9], v[18:25], v[174:177], v209, v208 op_sel_hi:[0,0,0]
	v_mfma_scale_f32_16x16x128_f8f6f4 v[170:173], v[10:17], v[18:25], v[170:173], v209, v208 op_sel_hi:[0,0,0]
	v_mfma_scale_f32_16x16x128_f8f6f4 v[166:169], v[2:9], v[26:33], v[166:169], v209, v208 op_sel_hi:[0,0,0]
	v_mfma_scale_f32_16x16x128_f8f6f4 v[162:165], v[10:17], v[26:33], v[162:165], v209, v208 op_sel_hi:[0,0,0]
	v_mfma_scale_f32_16x16x128_f8f6f4 v[142:145], v[2:9], v[34:41], v[222:225], v209, v208 op_sel_hi:[0,0,0]
	v_mfma_scale_f32_16x16x128_f8f6f4 v[138:141], v[10:17], v[34:41], v[226:229], v209, v208 op_sel_hi:[0,0,0]
	v_mfma_scale_f32_16x16x128_f8f6f4 v[134:137], v[2:9], v[42:49], v[134:137], v209, v208 op_sel_hi:[0,0,0]
	v_mfma_scale_f32_16x16x128_f8f6f4 v[122:125], v[10:17], v[42:49], v[122:125], v209, v208 op_sel_hi:[0,0,0]
	s_setprio 0
	s_barrier
	s_mov_b32 m0, s52
	v_add_u32_e32 v54, s51, v202
	v_lshl_add_u64 v[222:223], v[238:239], 0, s[8:9]
	v_add_u32_e32 v191, s51, v203
	ds_read_b128 v[50:53], v54
	ds_read_b128 v[214:217], v54 offset:2048
	ds_read_b128 v[54:57], v191
	ds_read_b128 v[218:221], v191 offset:2048
	global_load_lds_dwordx4 v[222:223], off
	v_lshl_add_u64 v[222:223], v[240:241], 0, s[8:9]
	s_mov_b32 m0, s53
	s_nop 0
	global_load_lds_dwordx4 v[222:223], off
	s_barrier
	s_setprio 1
	s_waitcnt lgkmcnt(0)
	v_mfma_scale_f32_16x16x128_f8f6f4 v[158:161], v[50:57], v[18:25], v[158:161], v209, v208 op_sel_hi:[0,0,0]
	v_mfma_scale_f32_16x16x128_f8f6f4 v[154:157], v[214:221], v[18:25], v[154:157], v209, v208 op_sel_hi:[0,0,0]
	ds_read_b128 v[18:21], v206 offset:49152
	ds_read_b128 v[22:25], v207 offset:49152
	v_mfma_scale_f32_16x16x128_f8f6f4 v[150:153], v[50:57], v[26:33], v[150:153], v209, v208 op_sel_hi:[0,0,0]
	v_mfma_scale_f32_16x16x128_f8f6f4 v[146:149], v[214:221], v[26:33], v[146:149], v209, v208 op_sel_hi:[0,0,0]
	ds_read_b128 v[26:29], v206 offset:51200
	ds_read_b128 v[30:33], v207 offset:51200
	v_mfma_scale_f32_16x16x128_f8f6f4 v[130:133], v[50:57], v[34:41], v[130:133], v209, v208 op_sel_hi:[0,0,0]
	v_mfma_scale_f32_16x16x128_f8f6f4 v[126:129], v[214:221], v[34:41], v[126:129], v209, v208 op_sel_hi:[0,0,0]
	ds_read_b128 v[34:37], v206 offset:53248
	ds_read_b128 v[38:41], v207 offset:53248
	v_mfma_scale_f32_16x16x128_f8f6f4 v[118:121], v[50:57], v[42:49], v[118:121], v209, v208 op_sel_hi:[0,0,0]
	v_mfma_scale_f32_16x16x128_f8f6f4 v[114:117], v[214:221], v[42:49], v[114:117], v209, v208 op_sel_hi:[0,0,0]
	ds_read_b128 v[42:45], v206 offset:55296
	ds_read_b128 v[46:49], v207 offset:55296
	s_setprio 0
	s_mov_b32 m0, s38
	v_lshl_add_u64 v[222:223], v[242:243], 0, s[8:9]
	s_barrier
	global_load_lds_dwordx4 v[222:223], off
	v_lshl_add_u64 v[222:223], v[244:245], 0, s[8:9]
	s_mov_b32 m0, s39
	s_nop 0
	global_load_lds_dwordx4 v[222:223], off
	s_barrier
	s_setprio 1
	s_waitcnt lgkmcnt(0)
	v_mfma_scale_f32_16x16x128_f8f6f4 v[110:113], v[2:9], v[18:25], v[110:113], v209, v208 op_sel_hi:[0,0,0]
	v_mfma_scale_f32_16x16x128_f8f6f4 v[106:109], v[10:17], v[18:25], v[106:109], v209, v208 op_sel_hi:[0,0,0]
	v_mfma_scale_f32_16x16x128_f8f6f4 v[102:105], v[2:9], v[26:33], v[102:105], v209, v208 op_sel_hi:[0,0,0]
	v_mfma_scale_f32_16x16x128_f8f6f4 v[98:101], v[10:17], v[26:33], v[98:101], v209, v208 op_sel_hi:[0,0,0]
	v_mfma_scale_f32_16x16x128_f8f6f4 v[78:81], v[2:9], v[34:41], v[78:81], v209, v208 op_sel_hi:[0,0,0]
	v_mfma_scale_f32_16x16x128_f8f6f4 v[74:77], v[10:17], v[34:41], v[74:77], v209, v208 op_sel_hi:[0,0,0]
	v_mfma_scale_f32_16x16x128_f8f6f4 v[70:73], v[2:9], v[42:49], v[70:73], v209, v208 op_sel_hi:[0,0,0]
	v_mfma_scale_f32_16x16x128_f8f6f4 v[66:69], v[10:17], v[42:49], v[66:69], v209, v208 op_sel_hi:[0,0,0]
	s_setprio 0
	s_barrier
	s_add_u32 s22, s22, 0x10080
	s_addc_u32 s23, s23, 0
	s_mov_b32 m0, s54
	v_lshl_add_u64 v[2:3], s[22:23], 0, v[188:189]
	global_load_lds_dwordx4 v[2:3], off
	v_lshl_add_u64 v[2:3], s[22:23], 0, v[186:187]
	s_add_i32 m0, s54, 0x2000
	s_nop 0
	global_load_lds_dwordx4 v[2:3], off
	s_waitcnt vmcnt(6)
	s_barrier
	s_setprio 1
	v_mfma_scale_f32_16x16x128_f8f6f4 v[94:97], v[50:57], v[18:25], v[94:97], v209, v208 op_sel_hi:[0,0,0]
	v_mfma_scale_f32_16x16x128_f8f6f4 v[90:93], v[214:221], v[18:25], v[90:93], v209, v208 op_sel_hi:[0,0,0]
	v_mfma_scale_f32_16x16x128_f8f6f4 v[86:89], v[50:57], v[26:33], v[86:89], v209, v208 op_sel_hi:[0,0,0]
	v_mfma_scale_f32_16x16x128_f8f6f4 v[82:85], v[214:221], v[26:33], v[82:85], v209, v208 op_sel_hi:[0,0,0]
	v_mfma_scale_f32_16x16x128_f8f6f4 v[62:65], v[50:57], v[34:41], v[62:65], v209, v208 op_sel_hi:[0,0,0]
	v_mfma_scale_f32_16x16x128_f8f6f4 v[58:61], v[214:221], v[34:41], v[58:61], v209, v208 op_sel_hi:[0,0,0]
	v_mfma_scale_f32_16x16x128_f8f6f4 v[54:57], v[50:57], v[42:49], v[230:233], v209, v208 op_sel_hi:[0,0,0]
	v_mfma_scale_f32_16x16x128_f8f6f4 v[50:53], v[214:221], v[42:49], v[234:237], v209, v208 op_sel_hi:[0,0,0]
	s_setprio 0
	s_cmp_ge_i32 s59, s1
	s_barrier
	s_cbranch_scc1 .LBB0_1668
	s_mov_b64 s[22:23], s[24:25]
	s_branch .LBB0_1673

.LBB0_1675:
	s_add_i32 s59, s59, 2
	s_add_u32 s24, s22, 0x100
	s_addc_u32 s25, s23, 0
	s_and_b64 s[28:29], s[26:27], exec
	s_cselect_b32 s28, 0, s24
	s_cselect_b32 s29, 0, s25
	s_add_u32 s28, s12, s28
	s_addc_u32 s29, s13, s29
	s_add_u32 s60, s57, s22
	s_addc_u32 s61, s58, s23
	s_and_b64 s[22:23], s[26:27], exec
	s_cselect_b32 s23, s55, s61
	s_cselect_b32 s22, s56, s60
	s_mov_b32 m0, s5
	s_waitcnt lgkmcnt(0)
	v_mfma_scale_f32_16x16x128_f8f6f4 v[222:225], v[2:9], v[42:49], v[142:145], v209, v208 op_sel_hi:[0,0,0]
	v_lshl_add_u64 v[238:239], s[22:23], 0, v[188:189]
	v_add_u32_e32 v191, s46, v203
	v_lshl_add_u64 v[240:241], s[22:23], 0, v[186:187]
	v_mov_b32_e32 v193, v185
	v_mov_b32_e32 v195, v185
	s_nop 1
	v_add_u32_e32 v142, s46, v202
	v_mfma_scale_f32_16x16x128_f8f6f4 v[226:229], v[10:17], v[42:49], v[138:141], v209, v208 op_sel_hi:[0,0,0]
	s_nop 6
	ds_read_b128 v[138:141], v142
	ds_read_b128 v[214:217], v142 offset:2048
	ds_read_b128 v[142:145], v191
	ds_read_b128 v[218:221], v191 offset:2048
	global_load_lds_dwordx4 v[238:239], off
	s_mov_b32 m0, s31
	s_nop 0
	global_load_lds_dwordx4 v[240:241], off
	v_mfma_scale_f32_16x16x128_f8f6f4 v[174:177], v[2:9], v[26:33], v[174:177], v209, v208 op_sel_hi:[0,0,0]
	s_barrier
	v_mfma_scale_f32_16x16x128_f8f6f4 v[170:173], v[10:17], v[26:33], v[170:173], v209, v208 op_sel_hi:[0,0,0]
	v_mfma_scale_f32_16x16x128_f8f6f4 v[166:169], v[2:9], v[18:25], v[166:169], v209, v208 op_sel_hi:[0,0,0]
	v_mfma_scale_f32_16x16x128_f8f6f4 v[162:165], v[10:17], v[18:25], v[162:165], v209, v208 op_sel_hi:[0,0,0]
	v_mfma_scale_f32_16x16x128_f8f6f4 v[134:137], v[2:9], v[34:41], v[134:137], v209, v208 op_sel_hi:[0,0,0]
	v_mfma_scale_f32_16x16x128_f8f6f4 v[122:125], v[10:17], v[34:41], v[122:125], v209, v208 op_sel_hi:[0,0,0]
	s_setprio 1
	s_waitcnt lgkmcnt(0)
	v_mfma_scale_f32_16x16x128_f8f6f4 v[158:161], v[138:145], v[26:33], v[158:161], v209, v208 op_sel_hi:[0,0,0]
	v_mfma_scale_f32_16x16x128_f8f6f4 v[154:157], v[214:221], v[26:33], v[154:157], v209, v208 op_sel_hi:[0,0,0]
	ds_read_b128 v[26:29], v206 offset:18432
	ds_read_b128 v[30:33], v207 offset:18432
	v_mfma_scale_f32_16x16x128_f8f6f4 v[150:153], v[138:145], v[18:25], v[150:153], v209, v208 op_sel_hi:[0,0,0]
	v_mfma_scale_f32_16x16x128_f8f6f4 v[146:149], v[214:221], v[18:25], v[146:149], v209, v208 op_sel_hi:[0,0,0]
	ds_read_b128 v[18:21], v206 offset:16384
	ds_read_b128 v[22:25], v207 offset:16384
	v_mfma_scale_f32_16x16x128_f8f6f4 v[130:133], v[138:145], v[42:49], v[130:133], v209, v208 op_sel_hi:[0,0,0]
	v_mfma_scale_f32_16x16x128_f8f6f4 v[126:129], v[214:221], v[42:49], v[126:129], v209, v208 op_sel_hi:[0,0,0]
	ds_read_b128 v[42:45], v206 offset:22528
	ds_read_b128 v[46:49], v207 offset:22528
	v_mfma_scale_f32_16x16x128_f8f6f4 v[118:121], v[138:145], v[34:41], v[118:121], v209, v208 op_sel_hi:[0,0,0]
	v_mfma_scale_f32_16x16x128_f8f6f4 v[114:117], v[214:221], v[34:41], v[114:117], v209, v208 op_sel_hi:[0,0,0]
	ds_read_b128 v[34:37], v206 offset:20480
	ds_read_b128 v[38:41], v207 offset:20480
	s_setprio 0
	s_mov_b32 m0, s4
	s_barrier
	global_load_lds_dwordx4 v184, s[28:29]
	s_mov_b32 m0, s33
	v_mov_b32_e32 v191, v185
	global_load_lds_dwordx4 v190, s[28:29]
	s_barrier
	v_lshl_add_u64 v[242:243], s[28:29], 0, v[184:185]
	v_lshl_add_u64 v[244:245], s[28:29], 0, v[190:191]
	s_setprio 1
	s_waitcnt lgkmcnt(0)
	v_mfma_scale_f32_16x16x128_f8f6f4 v[110:113], v[2:9], v[18:25], v[110:113], v209, v208 op_sel_hi:[0,0,0]
	v_mfma_scale_f32_16x16x128_f8f6f4 v[106:109], v[10:17], v[18:25], v[106:109], v209, v208 op_sel_hi:[0,0,0]
	v_mfma_scale_f32_16x16x128_f8f6f4 v[102:105], v[2:9], v[26:33], v[102:105], v209, v208 op_sel_hi:[0,0,0]
	v_mfma_scale_f32_16x16x128_f8f6f4 v[98:101], v[10:17], v[26:33], v[98:101], v209, v208 op_sel_hi:[0,0,0]
	v_mfma_scale_f32_16x16x128_f8f6f4 v[78:81], v[2:9], v[34:41], v[78:81], v209, v208 op_sel_hi:[0,0,0]
	v_mfma_scale_f32_16x16x128_f8f6f4 v[74:77], v[10:17], v[34:41], v[74:77], v209, v208 op_sel_hi:[0,0,0]
	v_mfma_scale_f32_16x16x128_f8f6f4 v[70:73], v[2:9], v[42:49], v[70:73], v209, v208 op_sel_hi:[0,0,0]
	v_mfma_scale_f32_16x16x128_f8f6f4 v[66:69], v[10:17], v[42:49], v[66:69], v209, v208 op_sel_hi:[0,0,0]
	s_setprio 0
	s_barrier
	s_add_u32 s26, s22, 0x10000
	s_addc_u32 s27, s23, 0
	s_mov_b32 m0, s48
	v_lshl_add_u64 v[2:3], s[26:27], 0, v[188:189]
	global_load_lds_dwordx4 v[2:3], off
	v_lshl_add_u64 v[2:3], s[26:27], 0, v[186:187]
	s_mov_b32 m0, s49
	s_nop 0
	global_load_lds_dwordx4 v[2:3], off
	s_waitcnt vmcnt(6)
	s_barrier
	s_setprio 1
	v_mfma_scale_f32_16x16x128_f8f6f4 v[94:97], v[138:145], v[18:25], v[94:97], v209, v208 op_sel_hi:[0,0,0]
	v_mfma_scale_f32_16x16x128_f8f6f4 v[90:93], v[214:221], v[18:25], v[90:93], v209, v208 op_sel_hi:[0,0,0]
	ds_read_b128 v[18:21], v206 offset:32768
	ds_read_b128 v[22:25], v207 offset:32768
	v_mfma_scale_f32_16x16x128_f8f6f4 v[86:89], v[138:145], v[26:33], v[86:89], v209, v208 op_sel_hi:[0,0,0]
	v_mfma_scale_f32_16x16x128_f8f6f4 v[82:85], v[214:221], v[26:33], v[82:85], v209, v208 op_sel_hi:[0,0,0]
	ds_read_b128 v[26:29], v206 offset:34816
	ds_read_b128 v[30:33], v207 offset:34816
	v_mfma_scale_f32_16x16x128_f8f6f4 v[62:65], v[138:145], v[34:41], v[62:65], v209, v208 op_sel_hi:[0,0,0]
	v_mfma_scale_f32_16x16x128_f8f6f4 v[58:61], v[214:221], v[34:41], v[58:61], v209, v208 op_sel_hi:[0,0,0]
	ds_read_b128 v[34:37], v206 offset:36864
	ds_read_b128 v[38:41], v207 offset:36864
	v_mfma_scale_f32_16x16x128_f8f6f4 v[230:233], v[138:145], v[42:49], v[54:57], v209, v208 op_sel_hi:[0,0,0]
	v_mfma_scale_f32_16x16x128_f8f6f4 v[234:237], v[214:221], v[42:49], v[50:53], v209, v208 op_sel_hi:[0,0,0]
	ds_read_b128 v[42:45], v206 offset:38912
	ds_read_b128 v[46:49], v207 offset:38912
	s_setprio 0
	v_add_u32_e32 v6, s50, v202
	v_add_u32_e32 v14, s50, v203
	s_barrier
	ds_read_b128 v[2:5], v6
	ds_read_b128 v[10:13], v6 offset:2048
	ds_read_b128 v[6:9], v14
	ds_read_b128 v[14:17], v14 offset:2048
	s_mov_b32 m0, s34
	v_lshl_add_u64 v[50:51], s[28:29], 0, v[192:193]
	global_load_lds_dwordx4 v[50:51], off
	v_lshl_add_u64 v[50:51], s[28:29], 0, v[194:195]
	s_mov_b32 m0, s35
	s_nop 0
	global_load_lds_dwordx4 v[50:51], off
	s_waitcnt lgkmcnt(8)
	s_barrier
	s_setprio 1
	s_waitcnt lgkmcnt(0)
	v_mfma_scale_f32_16x16x128_f8f6f4 v[174:177], v[2:9], v[18:25], v[174:177], v209, v208 op_sel_hi:[0,0,0]
	v_mfma_scale_f32_16x16x128_f8f6f4 v[170:173], v[10:17], v[18:25], v[170:173], v209, v208 op_sel_hi:[0,0,0]
	v_mfma_scale_f32_16x16x128_f8f6f4 v[166:169], v[2:9], v[26:33], v[166:169], v209, v208 op_sel_hi:[0,0,0]
	v_mfma_scale_f32_16x16x128_f8f6f4 v[162:165], v[10:17], v[26:33], v[162:165], v209, v208 op_sel_hi:[0,0,0]
	v_mfma_scale_f32_16x16x128_f8f6f4 v[142:145], v[2:9], v[34:41], v[222:225], v209, v208 op_sel_hi:[0,0,0]
	v_mfma_scale_f32_16x16x128_f8f6f4 v[138:141], v[10:17], v[34:41], v[226:229], v209, v208 op_sel_hi:[0,0,0]
	v_mfma_scale_f32_16x16x128_f8f6f4 v[134:137], v[2:9], v[42:49], v[134:137], v209, v208 op_sel_hi:[0,0,0]
	v_mfma_scale_f32_16x16x128_f8f6f4 v[122:125], v[10:17], v[42:49], v[122:125], v209, v208 op_sel_hi:[0,0,0]
	s_setprio 0
	s_barrier
	s_mov_b32 m0, s52
	v_add_u32_e32 v54, s51, v202
	v_lshl_add_u64 v[222:223], v[238:239], 0, s[8:9]
	v_add_u32_e32 v191, s51, v203
	ds_read_b128 v[50:53], v54
	ds_read_b128 v[214:217], v54 offset:2048
	ds_read_b128 v[54:57], v191
	ds_read_b128 v[218:221], v191 offset:2048
	global_load_lds_dwordx4 v[222:223], off
	v_lshl_add_u64 v[222:223], v[240:241], 0, s[8:9]
	s_mov_b32 m0, s53
	s_nop 0
	global_load_lds_dwordx4 v[222:223], off
	s_barrier
	s_setprio 1
	s_waitcnt lgkmcnt(0)
	v_mfma_scale_f32_16x16x128_f8f6f4 v[158:161], v[50:57], v[18:25], v[158:161], v209, v208 op_sel_hi:[0,0,0]
	v_mfma_scale_f32_16x16x128_f8f6f4 v[154:157], v[214:221], v[18:25], v[154:157], v209, v208 op_sel_hi:[0,0,0]
	ds_read_b128 v[18:21], v206 offset:49152
	ds_read_b128 v[22:25], v207 offset:49152
	v_mfma_scale_f32_16x16x128_f8f6f4 v[150:153], v[50:57], v[26:33], v[150:153], v209, v208 op_sel_hi:[0,0,0]
	v_mfma_scale_f32_16x16x128_f8f6f4 v[146:149], v[214:221], v[26:33], v[146:149], v209, v208 op_sel_hi:[0,0,0]
	ds_read_b128 v[26:29], v206 offset:51200
	ds_read_b128 v[30:33], v207 offset:51200
	v_mfma_scale_f32_16x16x128_f8f6f4 v[130:133], v[50:57], v[34:41], v[130:133], v209, v208 op_sel_hi:[0,0,0]
	v_mfma_scale_f32_16x16x128_f8f6f4 v[126:129], v[214:221], v[34:41], v[126:129], v209, v208 op_sel_hi:[0,0,0]
	ds_read_b128 v[34:37], v206 offset:53248
	ds_read_b128 v[38:41], v207 offset:53248
	v_mfma_scale_f32_16x16x128_f8f6f4 v[118:121], v[50:57], v[42:49], v[118:121], v209, v208 op_sel_hi:[0,0,0]
	v_mfma_scale_f32_16x16x128_f8f6f4 v[114:117], v[214:221], v[42:49], v[114:117], v209, v208 op_sel_hi:[0,0,0]
	ds_read_b128 v[42:45], v206 offset:55296
	ds_read_b128 v[46:49], v207 offset:55296
	s_setprio 0
	s_mov_b32 m0, s38
	v_lshl_add_u64 v[222:223], v[242:243], 0, s[8:9]
	s_barrier
	global_load_lds_dwordx4 v[222:223], off
	v_lshl_add_u64 v[222:223], v[244:245], 0, s[8:9]
	s_mov_b32 m0, s39
	s_nop 0
	global_load_lds_dwordx4 v[222:223], off
	s_barrier
	s_setprio 1
	s_waitcnt lgkmcnt(0)
	v_mfma_scale_f32_16x16x128_f8f6f4 v[110:113], v[2:9], v[18:25], v[110:113], v209, v208 op_sel_hi:[0,0,0]
	v_mfma_scale_f32_16x16x128_f8f6f4 v[106:109], v[10:17], v[18:25], v[106:109], v209, v208 op_sel_hi:[0,0,0]
	v_mfma_scale_f32_16x16x128_f8f6f4 v[102:105], v[2:9], v[26:33], v[102:105], v209, v208 op_sel_hi:[0,0,0]
	v_mfma_scale_f32_16x16x128_f8f6f4 v[98:101], v[10:17], v[26:33], v[98:101], v209, v208 op_sel_hi:[0,0,0]
	v_mfma_scale_f32_16x16x128_f8f6f4 v[78:81], v[2:9], v[34:41], v[78:81], v209, v208 op_sel_hi:[0,0,0]
	v_mfma_scale_f32_16x16x128_f8f6f4 v[74:77], v[10:17], v[34:41], v[74:77], v209, v208 op_sel_hi:[0,0,0]
	v_mfma_scale_f32_16x16x128_f8f6f4 v[70:73], v[2:9], v[42:49], v[70:73], v209, v208 op_sel_hi:[0,0,0]
	v_mfma_scale_f32_16x16x128_f8f6f4 v[66:69], v[10:17], v[42:49], v[66:69], v209, v208 op_sel_hi:[0,0,0]
	s_setprio 0
	s_barrier
	s_add_u32 s22, s22, 0x10080
	s_addc_u32 s23, s23, 0
	s_mov_b32 m0, s54
	v_lshl_add_u64 v[2:3], s[22:23], 0, v[188:189]
	global_load_lds_dwordx4 v[2:3], off
	v_lshl_add_u64 v[2:3], s[22:23], 0, v[186:187]
	s_add_i32 m0, s54, 0x2000
	s_nop 0
	global_load_lds_dwordx4 v[2:3], off
	s_waitcnt vmcnt(6)
	s_barrier
	s_setprio 1
	v_mfma_scale_f32_16x16x128_f8f6f4 v[94:97], v[50:57], v[18:25], v[94:97], v209, v208 op_sel_hi:[0,0,0]
	v_mfma_scale_f32_16x16x128_f8f6f4 v[90:93], v[214:221], v[18:25], v[90:93], v209, v208 op_sel_hi:[0,0,0]
	v_mfma_scale_f32_16x16x128_f8f6f4 v[86:89], v[50:57], v[26:33], v[86:89], v209, v208 op_sel_hi:[0,0,0]
	v_mfma_scale_f32_16x16x128_f8f6f4 v[82:85], v[214:221], v[26:33], v[82:85], v209, v208 op_sel_hi:[0,0,0]
	v_mfma_scale_f32_16x16x128_f8f6f4 v[62:65], v[50:57], v[34:41], v[62:65], v209, v208 op_sel_hi:[0,0,0]
	v_mfma_scale_f32_16x16x128_f8f6f4 v[58:61], v[214:221], v[34:41], v[58:61], v209, v208 op_sel_hi:[0,0,0]
	v_mfma_scale_f32_16x16x128_f8f6f4 v[54:57], v[50:57], v[42:49], v[230:233], v209, v208 op_sel_hi:[0,0,0]
	v_mfma_scale_f32_16x16x128_f8f6f4 v[50:53], v[214:221], v[42:49], v[234:237], v209, v208 op_sel_hi:[0,0,0]
	s_setprio 0
	s_cmp_ge_i32 s59, s1
	s_barrier
	s_cbranch_scc1 .LBB0_1668
	s_mov_b64 s[22:23], s[24:25]
	s_branch .LBB0_1673
